# speedup vs baseline: 1.0226x; 1.0226x over previous
.LBB1_34:
	s_or_b64 exec, exec, s[12:13]
	v_xor_b32_e32 v44, 16, v38
	v_lshlrev_b32_e32 v44, 2, v44
	v_xor_b32_e32 v45, 32, v38
	v_lshlrev_b32_e32 v45, 2, v45
	s_mov_b32 s12, 0x99999999
	s_mov_b32 s13, 0x99999999
	v_mov_b32_dpp v41, v19 quad_perm:[1,0,3,2] row_mask:0xf bank_mask:0xf
	v_min_u32_e32 v42, v19, v41
	v_max_u32_e32 v43, v19, v41
	v_cndmask_b32_e64 v19, v43, v42, s[12:13]
	s_mov_b32 s12, 0xc3c3c3c3
	s_mov_b32 s13, 0xc3c3c3c3
	v_mov_b32_dpp v41, v19 quad_perm:[2,3,0,1] row_mask:0xf bank_mask:0xf
	v_min_u32_e32 v42, v19, v41
	v_max_u32_e32 v43, v19, v41
	v_cndmask_b32_e64 v19, v43, v42, s[12:13]
	s_mov_b32 s12, 0xa5a5a5a5
	s_mov_b32 s13, 0xa5a5a5a5
	v_mov_b32_dpp v41, v19 quad_perm:[1,0,3,2] row_mask:0xf bank_mask:0xf
	v_min_u32_e32 v42, v19, v41
	v_max_u32_e32 v43, v19, v41
	v_cndmask_b32_e64 v19, v43, v42, s[12:13]
	s_mov_b32 s12, 0xf00ff00f
	s_mov_b32 s13, 0xf00ff00f
	v_mov_b32_dpp v41, v19 row_shl:4 row_mask:0xf bank_mask:0x5
	v_mov_b32_dpp v41, v19 row_shr:4 row_mask:0xf bank_mask:0xa
	v_min_u32_e32 v42, v19, v41
	v_max_u32_e32 v43, v19, v41
	v_cndmask_b32_e64 v19, v43, v42, s[12:13]
	s_mov_b32 s12, 0xcc33cc33
	s_mov_b32 s13, 0xcc33cc33
	v_mov_b32_dpp v41, v19 quad_perm:[2,3,0,1] row_mask:0xf bank_mask:0xf
	v_min_u32_e32 v42, v19, v41
	v_max_u32_e32 v43, v19, v41
	v_cndmask_b32_e64 v19, v43, v42, s[12:13]
	s_mov_b32 s12, 0xaa55aa55
	s_mov_b32 s13, 0xaa55aa55
	v_mov_b32_dpp v41, v19 quad_perm:[1,0,3,2] row_mask:0xf bank_mask:0xf
	v_min_u32_e32 v42, v19, v41
	v_max_u32_e32 v43, v19, v41
	v_cndmask_b32_e64 v19, v43, v42, s[12:13]
	s_mov_b32 s12, 0xff0000ff
	s_mov_b32 s13, 0xff0000ff
	v_mov_b32_dpp v41, v19 row_shl:8 row_mask:0xf bank_mask:0x3
	v_mov_b32_dpp v41, v19 row_shr:8 row_mask:0xf bank_mask:0xc
	v_min_u32_e32 v42, v19, v41
	v_max_u32_e32 v43, v19, v41
	v_cndmask_b32_e64 v19, v43, v42, s[12:13]
	s_mov_b32 s12, 0xf0f00f0f
	s_mov_b32 s13, 0xf0f00f0f
	v_mov_b32_dpp v41, v19 row_shl:4 row_mask:0xf bank_mask:0x5
	v_mov_b32_dpp v41, v19 row_shr:4 row_mask:0xf bank_mask:0xa
	v_min_u32_e32 v42, v19, v41
	v_max_u32_e32 v43, v19, v41
	v_cndmask_b32_e64 v19, v43, v42, s[12:13]
	s_mov_b32 s12, 0xcccc3333
	s_mov_b32 s13, 0xcccc3333
	v_mov_b32_dpp v41, v19 quad_perm:[2,3,0,1] row_mask:0xf bank_mask:0xf
	v_min_u32_e32 v42, v19, v41
	v_max_u32_e32 v43, v19, v41
	v_cndmask_b32_e64 v19, v43, v42, s[12:13]
	s_mov_b32 s12, 0xaaaa5555
	s_mov_b32 s13, 0xaaaa5555
	v_mov_b32_dpp v41, v19 quad_perm:[1,0,3,2] row_mask:0xf bank_mask:0xf
	v_min_u32_e32 v42, v19, v41
	v_max_u32_e32 v43, v19, v41
	v_cndmask_b32_e64 v19, v43, v42, s[12:13]
	s_mov_b32 s12, 0xffff
	s_mov_b32 s13, 0xffff0000
	ds_bpermute_b32 v41, v44, v19
	s_waitcnt lgkmcnt(0)
	v_min_u32_e32 v42, v19, v41
	v_max_u32_e32 v43, v19, v41
	v_cndmask_b32_e64 v19, v43, v42, s[12:13]
	s_mov_b32 s12, 0xff00ff
	s_mov_b32 s13, 0xff00ff00
	v_mov_b32_dpp v41, v19 row_shl:8 row_mask:0xf bank_mask:0x3
	v_mov_b32_dpp v41, v19 row_shr:8 row_mask:0xf bank_mask:0xc
	v_min_u32_e32 v42, v19, v41
	v_max_u32_e32 v43, v19, v41
	v_cndmask_b32_e64 v19, v43, v42, s[12:13]
	s_mov_b32 s12, 0xf0f0f0f
	s_mov_b32 s13, 0xf0f0f0f0
	v_mov_b32_dpp v41, v19 row_shl:4 row_mask:0xf bank_mask:0x5
	v_mov_b32_dpp v41, v19 row_shr:4 row_mask:0xf bank_mask:0xa
	v_min_u32_e32 v42, v19, v41
	v_max_u32_e32 v43, v19, v41
	v_cndmask_b32_e64 v19, v43, v42, s[12:13]
	s_mov_b32 s12, 0x33333333
	s_mov_b32 s13, 0xcccccccc
	v_mov_b32_dpp v41, v19 quad_perm:[2,3,0,1] row_mask:0xf bank_mask:0xf
	v_min_u32_e32 v42, v19, v41
	v_max_u32_e32 v43, v19, v41
	v_cndmask_b32_e64 v19, v43, v42, s[12:13]
	s_mov_b32 s12, 0x55555555
	s_mov_b32 s13, 0xaaaaaaaa
	v_mov_b32_dpp v41, v19 quad_perm:[1,0,3,2] row_mask:0xf bank_mask:0xf
	v_min_u32_e32 v42, v19, v41
	v_max_u32_e32 v43, v19, v41
	v_cndmask_b32_e64 v19, v43, v42, s[12:13]
	s_mov_b32 s12, 0xffffffff
	s_mov_b32 s13, 0x0
	ds_bpermute_b32 v41, v45, v19
	s_waitcnt lgkmcnt(0)
	v_min_u32_e32 v42, v19, v41
	v_max_u32_e32 v43, v19, v41
	v_cndmask_b32_e64 v19, v43, v42, s[12:13]
	s_mov_b32 s12, 0xffff
	s_mov_b32 s13, 0xffff
	ds_bpermute_b32 v41, v44, v19
	s_waitcnt lgkmcnt(0)
	v_min_u32_e32 v42, v19, v41
	v_max_u32_e32 v43, v19, v41
	v_cndmask_b32_e64 v19, v43, v42, s[12:13]
	s_mov_b32 s12, 0xff00ff
	s_mov_b32 s13, 0xff00ff
	v_mov_b32_dpp v41, v19 row_shl:8 row_mask:0xf bank_mask:0x3
	v_mov_b32_dpp v41, v19 row_shr:8 row_mask:0xf bank_mask:0xc
	v_min_u32_e32 v42, v19, v41
	v_max_u32_e32 v43, v19, v41
	v_cndmask_b32_e64 v19, v43, v42, s[12:13]
	s_mov_b32 s12, 0xf0f0f0f
	s_mov_b32 s13, 0xf0f0f0f
	v_mov_b32_dpp v41, v19 row_shl:4 row_mask:0xf bank_mask:0x5
	v_mov_b32_dpp v41, v19 row_shr:4 row_mask:0xf bank_mask:0xa
	v_min_u32_e32 v42, v19, v41
	v_max_u32_e32 v43, v19, v41
	v_cndmask_b32_e64 v19, v43, v42, s[12:13]
	s_mov_b32 s12, 0x33333333
	s_mov_b32 s13, 0x33333333
	v_mov_b32_dpp v41, v19 quad_perm:[2,3,0,1] row_mask:0xf bank_mask:0xf
	v_min_u32_e32 v42, v19, v41
	v_max_u32_e32 v43, v19, v41
	v_cndmask_b32_e64 v19, v43, v42, s[12:13]
	s_mov_b32 s12, 0x55555555
	s_mov_b32 s13, 0x55555555
	v_mov_b32_dpp v41, v19 quad_perm:[1,0,3,2] row_mask:0xf bank_mask:0xf
	v_min_u32_e32 v42, v19, v41
	v_max_u32_e32 v43, v19, v41
	v_cndmask_b32_e64 v19, v43, v42, s[12:13]
	v_sub_u32_e32 v39, 33, v38
	v_add_u32_e32 v42, 17, v38
	v_cmp_gt_u32_e64 s[12:13], 17, v38
	s_nop 1
	v_cndmask_b32_e64 v39, v42, v39, s[12:13]
	v_and_b32_e32 v39, 63, v39
	v_lshlrev_b32_e32 v39, 2, v39
	v_mov_b32_e32 v40, v19
	ds_bpermute_b32 v41, v39, v40
	v_lshl_or_b32 v39, s2, 2, v18
	s_movk_i32 s2, 0x3fd
	v_cmp_gt_i32_e64 s[2:3], s2, v39
	s_and_b64 s[2:3], s[10:11], s[2:3]
	s_and_b64 exec, exec, s[2:3]
	s_cbranch_execz .LBB1_38
	v_cmp_gt_u32_e64 s[2:3], 32, v38
	v_mov_b32_e32 v18, 0
	v_mov_b32_e32 v19, 0
	v_mov_b32_e32 v20, 0
	v_mov_b32_e32 v21, 0
	s_and_saveexec_b64 s[8:9], s[2:3]
	s_cbranch_execz .LBB1_37
	s_waitcnt lgkmcnt(0)
	v_cndmask_b32_e64 v42, v41, v40, s[12:13]
	v_mov_b32_e32 v18, 2
	s_nop 0
	v_lshlrev_b32_sdwa v19, v18, v42 dst_sel:DWORD dst_unused:UNUSED_PAD src0_sel:DWORD src1_sel:BYTE_0
	v_lshlrev_b32_sdwa v20, v18, v41 dst_sel:DWORD dst_unused:UNUSED_PAD src0_sel:DWORD src1_sel:BYTE_0
	ds_read_b32 v18, v19 offset:21504
	ds_read_b32 v20, v20 offset:21504
	v_lshrrev_b32_e32 v21, 8, v41
	v_lshrrev_b32_e32 v19, 8, v42
	v_cndmask_b32_e64 v21, 0, v21, s[12:13]

.LBB1_74:
	ds_read_b32 v10, v18 offset:19968
	v_ashrrev_i32_e32 v25, 31, v24
	v_lshlrev_b64 v[12:13], 7, v[24:25]
	s_waitcnt lgkmcnt(0)
	v_mul_f32_e32 v6, v10, v6
	v_mul_f32_e32 v7, v10, v7
	v_mul_f32_e32 v8, v10, v8
	v_mul_f32_e32 v9, v10, v9
	v_cvt_pk_f16_f32 v6, v6, v7
	v_cvt_pk_f16_f32 v7, v8, v9
	v_lshl_add_u64 v[8:9], v[0:1], 0, v[12:13]
	global_store_dwordx2 v[8:9], v[6:7], off
.LBB1_75:
	s_or_b64 exec, exec, s[0:1]
	s_movk_i32 s0, 0xc40
	v_cmp_gt_u32_e32 vcc, s0, v32
	v_cmp_gt_i32_e64 s[0:1], s2, v22
	s_and_b64 s[0:1], vcc, s[0:1]
	s_and_saveexec_b64 s[2:3], s[0:1]
	s_cbranch_execz .LBB1_77
	v_lshlrev_b32_e32 v6, 2, v23
	ds_read_b32 v6, v6 offset:19456
	v_ashrrev_i32_e32 v23, 31, v22
	v_lshlrev_b64 v[8:9], 7, v[22:23]
	v_lshl_add_u64 v[0:1], v[0:1], 0, v[8:9]
	s_waitcnt lgkmcnt(0)
	v_mul_f32_e32 v2, v6, v2
	v_mul_f32_e32 v3, v6, v3
	v_mul_f32_e32 v4, v6, v4
	v_mul_f32_e32 v5, v6, v5
	v_cvt_pk_f16_f32 v2, v2, v3
	v_cvt_pk_f16_f32 v3, v4, v5
	global_store_dwordx2 v[0:1], v[2:3], off

.LBB1_78:
	ds_read_b32 v20, v18 offset:19456
	v_ashrrev_i32_e32 v29, 31, v28
	v_lshlrev_b64 v[28:29], 7, v[28:29]
	s_waitcnt lgkmcnt(0)
	v_mul_f32_e32 v14, v20, v14
	v_mul_f32_e32 v15, v20, v15
	v_mul_f32_e32 v16, v20, v16
	v_mul_f32_e32 v17, v20, v17
	v_cvt_pk_f16_f32 v14, v14, v15
	v_cvt_pk_f16_f32 v15, v16, v17
	v_lshl_add_u64 v[16:17], v[0:1], 0, v[28:29]
	global_store_dwordx2 v[16:17], v[14:15], off
	s_or_b64 exec, exec, s[0:1]
	v_cmp_gt_i32_e32 vcc, s2, v26
	s_and_saveexec_b64 s[0:1], vcc
	s_cbranch_execz .LBB1_73
.LBB1_79:
	ds_read_b32 v14, v18 offset:19712
	v_ashrrev_i32_e32 v27, 31, v26
	v_lshlrev_b64 v[16:17], 7, v[26:27]
	s_waitcnt lgkmcnt(0)
	v_mul_f32_e32 v10, v14, v10
	v_mul_f32_e32 v11, v14, v11
	v_mul_f32_e32 v12, v14, v12
	v_mul_f32_e32 v13, v14, v13
	v_cvt_pk_f16_f32 v10, v10, v11
	v_cvt_pk_f16_f32 v11, v12, v13
	v_lshl_add_u64 v[12:13], v[0:1], 0, v[16:17]
	global_store_dwordx2 v[12:13], v[10:11], off
	s_or_b64 exec, exec, s[0:1]
	v_cmp_gt_i32_e32 vcc, s2, v24
	s_and_saveexec_b64 s[0:1], vcc
	s_cbranch_execnz .LBB1_74
	s_branch .LBB1_75

.LBB2_4:
	s_or_b64 exec, exec, s[6:7]
	s_load_dwordx2 s[10:11], s[0:1], 0x38
	s_waitcnt vmcnt(1)
	v_and_b32_e32 v121, 7, v0
	v_sub_co_u32_e32 v122, vcc, v121, v3
	v_add_u32_e32 v123, v2, v121
	v_add_u32_e32 v122, v122, v4
	v_cndmask_b32_e32 v122, v122, v123, vcc
	v_mov_b32_e32 v123, 0
	v_lshl_add_u64 v[122:123], v[122:123], 2, s[12:13]
	global_load_dword v120, v[122:123], off
	v_div_scale_f32 v15, s[0:1], v17, v17, 1.0
	v_rcp_f32_e32 v18, v15
	v_and_b32_e32 v89, 7, v0
	v_cvt_f32_f16_sdwa v23, v11 dst_sel:DWORD dst_unused:UNUSED_PAD src0_sel:WORD_1
	v_cvt_f32_f16_e32 v22, v11
	v_fma_f32 v19, -v15, v18, 1.0
	v_fmac_f32_e32 v18, v19, v18
	v_div_scale_f32 v19, vcc, 1.0, v17, 1.0
	v_mul_f32_e32 v20, v19, v18
	v_fma_f32 v21, -v15, v20, v19
	v_fmac_f32_e32 v20, v21, v18
	v_fma_f32 v15, -v15, v20, v19
	s_waitcnt vmcnt(1)
	v_div_scale_f32 v19, s[0:1], v14, v14, 1.0
	v_rcp_f32_e32 v21, v19
	v_div_fmas_f32 v15, v15, v18, v20
	v_div_fixup_f32 v18, v15, v17, 1.0
	v_cvt_f32_f16_sdwa v11, v12 dst_sel:DWORD dst_unused:UNUSED_PAD src0_sel:WORD_1
	v_fma_f32 v15, -v19, v21, 1.0
	v_fmac_f32_e32 v21, v15, v21
	v_div_scale_f32 v15, vcc, 1.0, v14, 1.0
	v_mul_f32_e32 v17, v15, v21
	v_fma_f32 v20, -v19, v17, v15
	v_fmac_f32_e32 v17, v20, v21
	v_fma_f32 v15, -v19, v17, v15
	v_div_fmas_f32 v15, v15, v21, v17
	v_cvt_f32_f16_sdwa v21, v10 dst_sel:DWORD dst_unused:UNUSED_PAD src0_sel:WORD_1
	v_cvt_f32_f16_e32 v20, v10
	v_cvt_f32_f16_e32 v10, v12
	v_cvt_f32_f16_sdwa v25, v13 dst_sel:DWORD dst_unused:UNUSED_PAD src0_sel:WORD_1
	v_cvt_f32_f16_e32 v24, v13
	v_cvt_f32_f16_sdwa v13, v6 dst_sel:DWORD dst_unused:UNUSED_PAD src0_sel:WORD_1
	v_cvt_f32_f16_e32 v12, v6
	v_lshlrev_b32_e32 v84, 2, v89
	v_mul_u32_u24_e32 v87, 0x120, v1
	v_cvt_f32_f16_sdwa v27, v7 dst_sel:DWORD dst_unused:UNUSED_PAD src0_sel:WORD_1
	v_cvt_f32_f16_e32 v26, v7
	v_div_fixup_f32 v14, v15, v14, 1.0
	v_or_b32_e32 v15, v84, v87
	v_mul_u32_u24_e32 v85, 0x120, v71
	v_cvt_f32_f16_sdwa v29, v8 dst_sel:DWORD dst_unused:UNUSED_PAD src0_sel:WORD_1
	v_cvt_f32_f16_e32 v28, v8
	ds_write2_b32 v15, v20, v21 offset1:8
	ds_write2_b32 v15, v22, v23 offset0:16 offset1:24
	ds_write2_b32 v15, v10, v11 offset0:32 offset1:40
	ds_write2_b32 v15, v24, v25 offset0:48 offset1:56
	v_or_b32_e32 v15, v84, v85
	v_cvt_f32_f16_sdwa v31, v9 dst_sel:DWORD dst_unused:UNUSED_PAD src0_sel:WORD_1
	v_cvt_f32_f16_e32 v30, v9
	v_mov_b32_e32 v6, 0x4800
	ds_write2_b32 v15, v12, v13 offset1:8
	ds_write2_b32 v15, v26, v27 offset0:16 offset1:24
	ds_write2_b32 v15, v28, v29 offset0:32 offset1:40
	ds_write2_b32 v15, v30, v31 offset0:48 offset1:56
	v_lshl_or_b32 v15, v16, 1, v6
	v_mul_f32_e32 v6, v18, v20
	v_mul_f32_e32 v7, v18, v21
	v_mul_f32_e32 v8, v18, v22
	v_mul_f32_e32 v9, v18, v23
	v_cvt_pk_f16_f32 v6, v6, v7
	v_cvt_pk_f16_f32 v7, v8, v9
	v_mul_f32_e32 v8, v18, v10
	v_mul_f32_e32 v9, v18, v11
	v_mul_f32_e32 v10, v18, v24
	v_mul_f32_e32 v11, v18, v25
	s_movk_i32 s0, 0x110
	v_cvt_pk_f16_f32 v8, v8, v9
	v_cvt_pk_f16_f32 v9, v10, v11
	v_mad_u32_u24 v88, v1, s0, v15
	ds_write_b128 v88, v[6:9] offset:128
	v_mul_f32_e32 v6, v14, v12
	v_mul_f32_e32 v7, v14, v13
	v_mul_f32_e32 v8, v14, v26
	v_mul_f32_e32 v9, v14, v27
	v_cvt_pk_f16_f32 v6, v6, v7
	v_cvt_pk_f16_f32 v7, v8, v9
	v_mul_f32_e32 v8, v14, v28
	v_mul_f32_e32 v9, v14, v29
	v_mul_f32_e32 v10, v14, v30
	v_mul_f32_e32 v11, v14, v31
	v_and_b32_e32 v82, 63, v0
	v_cvt_pk_f16_f32 v8, v8, v9
	v_cvt_pk_f16_f32 v9, v10, v11
	v_mad_u32_u24 v86, v71, s0, v15
	v_lshrrev_b32_e32 v73, 6, v0
	ds_write_b128 v86, v[6:9] offset:128
	v_lshlrev_b32_e32 v6, 4, v82
	v_lshl_or_b32 v74, v73, 13, v6
	v_mov_b32_e32 v75, 0
	s_waitcnt lgkmcnt(0)
	v_lshl_add_u64 v[6:7], s[16:17], 0, v[74:75]
	s_movk_i32 s0, 0x1000
	v_add_co_u32_e32 v6, vcc, s0, v6
	s_nop 1
	v_addc_co_u32_e32 v7, vcc, 0, v7, vcc
	s_barrier
	global_load_dwordx4 v[62:65], v74, s[16:17]
	global_load_dwordx4 v[58:61], v74, s[16:17] offset:1024
	global_load_dwordx4 v[54:57], v74, s[16:17] offset:2048
	global_load_dwordx4 v[50:53], v74, s[16:17] offset:3072
	global_load_dwordx4 v[46:49], v[6:7], off
	global_load_dwordx4 v[42:45], v[6:7], off offset:1024
	global_load_dwordx4 v[38:41], v[6:7], off offset:2048
	global_load_dwordx4 v[34:37], v[6:7], off offset:3072
	s_setprio 2
	v_mbcnt_lo_u32_b32 v7, -1, 0
	v_add_u32_e32 v5, v5, v3
	v_mbcnt_hi_u32_b32 v83, -1, v7
	v_mov_b32_e32 v90, 0x100c350
	v_lshlrev_b32_e32 v14, 2, v83
	v_cmp_lt_u32_e32 vcc, v89, v5
	v_and_b32_e32 v91, 0x1e0, v14
	v_add_u32_e32 v15, 7, v5
	v_lshlrev_b32_e32 v74, 4, v89
	v_mov_b32_e32 v103, v75
	v_mov_b32_e32 v105, v75
	v_mov_b32_e32 v106, v75
	v_mov_b32_e32 v108, v75
	v_mov_b32_e32 v110, v75
	v_mov_b32_e32 v111, v75
	v_mov_b32_e32 v112, v75
	s_waitcnt vmcnt(8)
	v_cndmask_b32_e32 v101, v90, v120, vcc
	ds_bpermute_b32 v9, v91, v101
	ds_bpermute_b32 v8, v91, v101 offset:4
	ds_bpermute_b32 v7, v91, v101 offset:8
	ds_bpermute_b32 v6, v91, v101 offset:12
	v_cmp_lt_u32_e32 vcc, 7, v15
	s_waitcnt lgkmcnt(3)
	v_lshrrev_b32_e32 v109, 16, v9
	s_and_saveexec_b64 s[14:15], vcc
	s_cbranch_execz .LBB2_24
	v_mov_b32_e32 v77, 0
	v_mov_b32_e32 v75, v77
	v_lshlrev_b32_e32 v9, 7, v9
	v_lshl_add_u64 v[78:79], s[8:9], 0, v[74:75]
	v_and_b32_e32 v76, 0x7fff80, v9
	s_waitcnt lgkmcnt(2)
	v_lshlrev_b32_e32 v8, 7, v8
	v_lshl_add_u64 v[10:11], v[78:79], 0, v[76:77]
	v_and_b32_e32 v76, 0x7fff80, v8
	s_waitcnt lgkmcnt(1)
	v_lshlrev_b32_e32 v7, 7, v7
	v_or_b32_e32 v16, 8, v89
	v_lshl_add_u64 v[8:9], v[78:79], 0, v[76:77]
	global_load_dwordx4 v[26:29], v[10:11], off
	global_load_dwordx4 v[18:21], v[8:9], off
	v_and_b32_e32 v76, 0x7fff80, v7
	s_waitcnt lgkmcnt(0)
	v_lshlrev_b32_e32 v6, 7, v6
	v_sub_co_u32_e32 v11, vcc, v16, v3
	v_lshl_add_u64 v[8:9], v[78:79], 0, v[76:77]
	v_and_b32_e32 v76, 0x7fff80, v6
	v_add_u32_e32 v10, v2, v16
	v_add_u32_e32 v11, v11, v4
	v_lshl_add_u64 v[6:7], v[78:79], 0, v[76:77]
	v_cndmask_b32_e32 v76, v11, v10, vcc
	v_lshl_add_u64 v[10:11], v[76:77], 2, s[12:13]
	global_load_dword v17, v[10:11], off
	s_nop 0
	global_load_dwordx4 v[10:13], v[8:9], off
	s_nop 0
	global_load_dwordx4 v[6:9], v[6:7], off
	v_cmp_lt_u32_e64 s[0:1], v16, v5
	v_or_b32_e32 v92, 4, v91
	v_or_b32_e32 v93, 8, v91
	v_or_b32_e32 v94, 12, v91
	v_lshrrev_b32_e32 v95, 3, v15
	v_sub_u32_e32 v96, v4, v3
	v_cmp_eq_u32_e32 vcc, 0, v89
	v_and_b32_e32 v4, 56, v83
	v_or_b32_e32 v97, 16, v91
	v_or_b32_e32 v98, 20, v91
	v_or_b32_e32 v99, 24, v91
	v_or_b32_e32 v100, 28, v14
	v_or_b32_e32 v102, 16, v89
	s_mov_b64 s[8:9], 0
	s_mov_b32 s16, 0x1000000
	v_mov_b32_e32 v112, 0
	v_mov_b32_e32 v111, 0
	v_mov_b32_e32 v110, 0
	v_mov_b32_e32 v108, 0
	v_mov_b32_e32 v106, 0
	v_mov_b32_e32 v105, 0
	v_mov_b32_e32 v103, 0
	v_mov_b32_e32 v75, 0
	s_waitcnt vmcnt(2)
	v_cndmask_b32_e64 v104, v90, v17, s[0:1]
	s_branch .LBB2_7

.LBB2_26:
	s_or_b64 exec, exec, s[0:1]
	s_waitcnt vmcnt(2)
	v_lshrrev_b32_e32 v18, 5, v82
	s_waitcnt vmcnt(0)
	v_lshlrev_b32_e32 v9, 5, v73
	v_and_b32_e32 v66, 31, v0
	s_setprio 0
	v_lshlrev_b32_e32 v2, 2, v1
	s_waitcnt lgkmcnt(1)
	v_add_u32_e32 v7, v84, v87
	s_waitcnt lgkmcnt(0)
	s_barrier
	ds_read_b32 v6, v2 offset:35840
	ds_read2_b32 v[2:3], v7 offset1:8
	ds_read2_b32 v[4:5], v7 offset0:16 offset1:24
	ds_read2_b32 v[10:11], v7 offset0:32 offset1:40
	v_lshlrev_b32_e32 v8, 2, v71
	ds_read_b32 v8, v8 offset:35840
	s_waitcnt lgkmcnt(3)
	v_fma_mixlo_f16 v12, v6, v2, 0
	v_mov_b32_e32 v2, v3
	s_waitcnt lgkmcnt(2)
	v_mov_b32_e32 v3, v4
	v_mul_f32_e32 v2, v6, v2
	v_mul_f32_e32 v3, v6, v3
	v_cvt_pk_f16_f32 v3, v2, v3
	v_pack_b32_f16 v2, v12, v3
	ds_read2_b32 v[12:13], v7 offset0:48 offset1:56
	v_mov_b32_e32 v4, v5
	s_waitcnt lgkmcnt(2)
	v_mov_b32_e32 v5, v10
	v_mul_f32_e32 v4, v6, v4
	v_mul_f32_e32 v5, v6, v5
	v_cvt_pk_f16_f32 v7, v4, v5
	s_waitcnt lgkmcnt(0)
	v_mov_b32_e32 v5, v12
	v_add_u32_e32 v12, v84, v85
	v_mov_b32_e32 v4, v11
	ds_read2_b32 v[10:11], v12 offset1:8
	v_mul_f32_e32 v4, v6, v4
	v_mul_f32_e32 v5, v6, v5
	v_cvt_pk_f16_f32 v5, v4, v5
	ds_read2_b32 v[14:15], v12 offset0:16 offset1:24
	v_alignbit_b32 v4, v5, v7, 16
	v_lshrrev_b32_e32 v5, 16, v5
	v_alignbit_b32 v3, v7, v3, 16
	v_fma_mixhi_f16 v5, v6, v13, 0
	ds_write_b128 v88, v[2:5]
	s_waitcnt lgkmcnt(2)
	v_fma_mixlo_f16 v6, v8, v10, 0
	v_mov_b32_e32 v2, v11
	ds_read2_b32 v[4:5], v12 offset0:32 offset1:40
	ds_read2_b32 v[10:11], v12 offset0:48 offset1:56
	s_waitcnt lgkmcnt(3)
	v_mov_b32_e32 v3, v14
	v_mul_f32_e32 v2, v8, v2
	v_mul_f32_e32 v3, v8, v3
	v_cvt_pk_f16_f32 v3, v2, v3
	v_pack_b32_f16 v2, v6, v3
	v_mov_b32_e32 v6, v15
	s_waitcnt lgkmcnt(1)
	v_mov_b32_e32 v7, v4
	v_mov_b32_e32 v4, v5
	s_waitcnt lgkmcnt(0)
	v_mov_b32_e32 v5, v10
	v_mul_f32_e32 v6, v8, v6
	v_mul_f32_e32 v7, v8, v7
	v_mul_f32_e32 v4, v8, v4
	v_mul_f32_e32 v5, v8, v5
	v_cvt_pk_f16_f32 v6, v6, v7
	v_cvt_pk_f16_f32 v5, v4, v5
	v_alignbit_b32 v4, v5, v6, 16
	v_lshrrev_b32_e32 v5, 16, v5
	v_lshl_or_b32 v67, v18, 2, v9
	v_alignbit_b32 v3, v6, v3, 16
	v_fma_mixhi_f16 v5, v8, v11, 0
	v_lshlrev_b32_e32 v19, 2, v67
	ds_write_b128 v86, v[2:5]
	s_waitcnt lgkmcnt(0)
	s_barrier
	global_load_dwordx4 v[2:5], v19, s[18:19]
	global_load_dwordx4 v[6:9], v19, s[18:19] offset:32
	global_load_dwordx4 v[10:13], v19, s[18:19] offset:64
	global_load_dwordx4 v[14:17], v19, s[18:19] offset:96
	v_lshlrev_b32_e32 v18, 4, v18
	s_movk_i32 s0, 0x110
	v_mad_u32_u24 v68, v66, s0, v18
	ds_read_b128 v[76:79], v68 offset:18432
	ds_read_b128 v[84:87], v68 offset:18464
	s_waitcnt vmcnt(0) lgkmcnt(1)
	v_mfma_f32_32x32x16_f16 v[18:33], v[62:65], v[76:79], v[2:17]
	ds_read_b128 v[76:79], v68 offset:27136
	ds_read_b128 v[88:91], v68 offset:27168
	s_waitcnt lgkmcnt(1)
	v_mfma_f32_32x32x16_f16 v[2:17], v[62:65], v[76:79], v[2:17]
	v_mfma_f32_32x32x16_f16 v[18:33], v[58:61], v[84:87], v[18:33]
	s_waitcnt lgkmcnt(0)
	v_mfma_f32_32x32x16_f16 v[2:17], v[58:61], v[88:91], v[2:17]
	ds_read_b128 v[58:61], v68 offset:18496
	ds_read_b128 v[62:65], v68 offset:18528
	s_waitcnt lgkmcnt(1)
	v_mfma_f32_32x32x16_f16 v[18:33], v[54:57], v[58:61], v[18:33]
	ds_read_b128 v[58:61], v68 offset:27200
	ds_read_b128 v[76:79], v68 offset:27232
	s_waitcnt lgkmcnt(1)
	v_mfma_f32_32x32x16_f16 v[2:17], v[54:57], v[58:61], v[2:17]
	v_mfma_f32_32x32x16_f16 v[18:33], v[50:53], v[62:65], v[18:33]
	s_waitcnt lgkmcnt(0)
	v_mfma_f32_32x32x16_f16 v[2:17], v[50:53], v[76:79], v[2:17]
	ds_read_b128 v[50:53], v68 offset:18560
	ds_read_b128 v[54:57], v68 offset:18592
	s_waitcnt lgkmcnt(1)
	v_mfma_f32_32x32x16_f16 v[18:33], v[46:49], v[50:53], v[18:33]
	ds_read_b128 v[50:53], v68 offset:27264
	ds_read_b128 v[58:61], v68 offset:27296
	s_waitcnt lgkmcnt(1)
	v_mfma_f32_32x32x16_f16 v[2:17], v[46:49], v[50:53], v[2:17]
	v_mfma_f32_32x32x16_f16 v[18:33], v[42:45], v[54:57], v[18:33]
	s_waitcnt lgkmcnt(0)
	v_mfma_f32_32x32x16_f16 v[2:17], v[42:45], v[58:61], v[2:17]
	ds_read_b128 v[42:45], v68 offset:18624
	ds_read_b128 v[46:49], v68 offset:18656
	s_waitcnt lgkmcnt(1)
	v_mfma_f32_32x32x16_f16 v[18:33], v[38:41], v[42:45], v[18:33]
	ds_read_b128 v[42:45], v68 offset:27328
	ds_read_b128 v[50:53], v68 offset:27360
	s_waitcnt lgkmcnt(1)
	v_mfma_f32_32x32x16_f16 v[2:17], v[38:41], v[42:45], v[2:17]
	v_lshlrev_b32_e32 v38, 2, v66
	v_add_u32_e32 v38, 0x8c00, v38
	ds_read2_b32 v[38:39], v38 offset1:32
	v_mfma_f32_32x32x16_f16 v[18:33], v[34:37], v[46:49], v[18:33]
	s_waitcnt lgkmcnt(1)
	v_mfma_f32_32x32x16_f16 v[2:17], v[34:37], v[50:53], v[2:17]
	s_nop 9
	v_max_f32_e32 v18, v18, v18
	v_max_f32_e32 v19, v19, v19
	v_max_f32_e32 v20, v20, v20
	v_max_f32_e32 v21, v21, v21
	v_max_f32_e32 v18, 0, v18
	v_max_f32_e32 v19, 0, v19
	v_max_f32_e32 v22, v22, v22
	v_max_f32_e32 v2, v2, v2
	v_max_f32_e32 v3, v3, v3
	v_max_f32_e32 v4, v4, v4
	v_max_f32_e32 v5, v5, v5
	v_max_f32_e32 v7, v7, v7
	v_max_f32_e32 v2, 0, v2
	v_max_f32_e32 v3, 0, v3
	v_max_f32_e32 v6, v6, v6
	v_max_f32_e32 v23, v23, v23
	v_max_f32_e32 v8, v8, v8
	v_max_f32_e32 v9, v9, v9
	v_max_f32_e32 v20, 0, v20
	v_max_f32_e32 v4, 0, v4
	v_max_f32_e32 v21, 0, v21
	v_max_f32_e32 v5, 0, v5
	v_max_f32_e32 v7, 0, v7
	s_waitcnt lgkmcnt(0)
	v_mul_f32_e32 v42, v38, v18
	v_mul_f32_e32 v41, v39, v2
	v_mul_f32_e32 v40, v38, v19
	v_mul_f32_e32 v37, v39, v3
	v_max_f32_e32 v24, v24, v24
	v_max_f32_e32 v25, v25, v25
	v_max_f32_e32 v43, v26, v26
	v_max_f32_e32 v22, 0, v22
	v_max_f32_e32 v6, 0, v6
	v_max_f32_e32 v23, 0, v23
	v_max_f32_e32 v8, 0, v8
	v_max_f32_e32 v9, 0, v9
	v_mul_f32_e32 v36, v38, v20
	v_mul_f32_e32 v35, v39, v4
	v_mul_f32_e32 v34, v38, v21
	v_mul_f32_e32 v26, v39, v5
	v_mul_f32_e32 v19, v39, v7
	v_max_f32_e32 v5, v42, v41
	v_max_f32_e32 v7, v40, v37
	v_max_f32_e32 v44, 0, v24
	v_max_f32_e32 v45, 0, v25
	v_mul_f32_e32 v25, v38, v22
	v_mul_f32_e32 v24, v39, v6
	v_mul_f32_e32 v20, v38, v23
	v_mul_f32_e32 v4, v39, v8
	v_mul_f32_e32 v2, v39, v9
	v_max_f32_e32 v8, v36, v35
	v_max_f32_e32 v9, v34, v26
	v_max3_f32 v5, v5, 0, v7
	v_mul_f32_e32 v6, v38, v44
	v_mul_f32_e32 v3, v38, v45
	v_max_f32_e32 v18, v25, v24
	v_max_f32_e32 v21, v20, v19
	v_max3_f32 v5, v5, v8, v9
	v_max_f32_e32 v22, v6, v4
	v_max_f32_e32 v23, v3, v2
	v_max3_f32 v5, v5, v18, v21
	v_max_f32_e32 v7, v10, v10
	v_max_f32_e32 v8, v27, v27
	v_max_f32_e32 v9, v11, v11
	v_max3_f32 v18, v5, v22, v23
	v_max_f32_e32 v5, 0, v43
	v_max_f32_e32 v7, 0, v7
	v_max_f32_e32 v8, 0, v8
	v_max_f32_e32 v9, 0, v9
	v_mul_f32_e32 v5, v38, v5
	v_mul_f32_e32 v7, v39, v7
	v_mul_f32_e32 v8, v38, v8
	v_mul_f32_e32 v9, v39, v9
	v_max_f32_e32 v10, v5, v7
	v_max_f32_e32 v11, v8, v9
	v_max3_f32 v21, v18, v10, v11
	v_max_f32_e32 v10, v28, v28
	v_max_f32_e32 v10, 0, v10
	v_mul_f32_e32 v18, v38, v10
	v_max_f32_e32 v10, v12, v12
	v_max_f32_e32 v10, 0, v10
	v_mul_f32_e32 v12, v39, v10
	v_max_f32_e32 v10, v29, v29
	v_max_f32_e32 v11, v13, v13
	v_max_f32_e32 v10, 0, v10
	v_max_f32_e32 v11, 0, v11
	v_mul_f32_e32 v10, v38, v10
	v_mul_f32_e32 v11, v39, v11
	v_max_f32_e32 v22, v18, v12
	v_max_f32_e32 v13, v10, v11
	v_max3_f32 v23, v21, v22, v13
	v_max_f32_e32 v13, v30, v30
	v_max_f32_e32 v14, v14, v14
	v_max_f32_e32 v21, v31, v31
	v_max_f32_e32 v15, v15, v15
	v_max_f32_e32 v13, 0, v13
	v_max_f32_e32 v14, 0, v14
	v_max_f32_e32 v21, 0, v21
	v_max_f32_e32 v15, 0, v15
	v_mul_f32_e32 v13, v38, v13
	v_mul_f32_e32 v14, v39, v14
	v_mul_f32_e32 v21, v38, v21
	v_mul_f32_e32 v22, v39, v15
	v_max_f32_e32 v27, v13, v14
	v_max_f32_e32 v15, v21, v22
	v_max3_f32 v27, v23, v27, v15
	v_max_f32_e32 v15, v32, v32
	v_max_f32_e32 v16, v16, v16
	v_max_f32_e32 v23, v33, v33
	v_max_f32_e32 v17, v17, v17
	v_max_f32_e32 v15, 0, v15
	v_max_f32_e32 v16, 0, v16
	v_max_f32_e32 v23, 0, v23
	v_max_f32_e32 v17, 0, v17
	v_mul_f32_e32 v15, v38, v15
	v_mul_f32_e32 v16, v39, v16
	v_mul_f32_e32 v23, v38, v23
	v_mul_f32_e32 v17, v39, v17
	v_max_f32_e32 v28, v15, v16
	v_max_f32_e32 v29, v23, v17
	v_max3_f32 v27, v27, v28, v29
	v_and_b32_e32 v28, 64, v83
	v_add_u32_e32 v28, 64, v28
	v_xor_b32_e32 v29, 32, v83
	v_cmp_lt_i32_e32 vcc, v29, v28
	s_nop 1
	v_cndmask_b32_e32 v29, v83, v29, vcc
	v_lshlrev_b32_e32 v29, 2, v29
	ds_bpermute_b32 v29, v29, v27
	s_waitcnt lgkmcnt(0)
	v_max_f32_e32 v29, v29, v29
	v_max_f32_e32 v27, v27, v29
	v_xor_b32_e32 v29, 16, v83
	v_cmp_lt_i32_e32 vcc, v29, v28
	s_nop 1
	v_cndmask_b32_e32 v29, v83, v29, vcc
	v_lshlrev_b32_e32 v29, 2, v29
	ds_bpermute_b32 v29, v29, v27
	s_waitcnt lgkmcnt(0)
	v_max_f32_e32 v29, v29, v29
	v_max_f32_e32 v27, v27, v29
	v_xor_b32_e32 v29, 8, v83
	v_cmp_lt_i32_e32 vcc, v29, v28
	s_nop 1
	v_cndmask_b32_e32 v29, v83, v29, vcc
	v_lshlrev_b32_e32 v29, 2, v29
	ds_bpermute_b32 v29, v29, v27
	s_waitcnt lgkmcnt(0)
	v_max_f32_e32 v29, v29, v29
	v_max_f32_e32 v27, v27, v29
	v_xor_b32_e32 v29, 4, v83
	v_cmp_lt_i32_e32 vcc, v29, v28
	s_nop 1
	v_cndmask_b32_e32 v29, v83, v29, vcc
	v_lshlrev_b32_e32 v29, 2, v29
	ds_bpermute_b32 v29, v29, v27
	s_waitcnt lgkmcnt(0)
	v_max_f32_e32 v29, v29, v29
	v_max_f32_e32 v27, v27, v29
	v_xor_b32_e32 v29, 2, v83
	v_cmp_lt_i32_e32 vcc, v29, v28
	s_nop 1
	v_cndmask_b32_e32 v29, v83, v29, vcc
	v_lshlrev_b32_e32 v29, 2, v29
	ds_bpermute_b32 v29, v29, v27
	s_waitcnt lgkmcnt(0)
	v_max_f32_e32 v29, v29, v29
	v_max_f32_e32 v27, v27, v29
	v_xor_b32_e32 v29, 1, v83
	v_cmp_lt_i32_e32 vcc, v29, v28
	s_nop 1
	v_cndmask_b32_e32 v28, v83, v29, vcc
	v_lshlrev_b32_e32 v28, 2, v28
	ds_bpermute_b32 v28, v28, v27
	v_cmp_eq_u32_e32 vcc, 0, v82
	s_and_saveexec_b64 s[0:1], vcc
	s_cbranch_execz .LBB2_28
	s_waitcnt lgkmcnt(0)
	v_max_f32_e32 v28, v28, v28
	v_max_f32_e32 v27, v27, v27
	v_max_f32_e32 v27, v27, v28
	v_lshlrev_b32_e32 v28, 2, v73
	ds_write_b32 v28, v27 offset:36096

	.amdhsa_kernel _Z8k_layer1PKfPKDF16_PK15HIP_vector_typeIjLj4EEPKjS0_S2_S0_PhPf
		.amdhsa_group_segment_fixed_size 36112
		.amdhsa_private_segment_fixed_size 0
		.amdhsa_kernarg_size 72
		.amdhsa_user_sgpr_count 2
		.amdhsa_user_sgpr_dispatch_ptr 0
		.amdhsa_user_sgpr_queue_ptr 0
		.amdhsa_user_sgpr_kernarg_segment_ptr 1
		.amdhsa_user_sgpr_dispatch_id 0
		.amdhsa_user_sgpr_kernarg_preload_length 0
		.amdhsa_user_sgpr_kernarg_preload_offset 0
		.amdhsa_user_sgpr_private_segment_size 0
		.amdhsa_uses_dynamic_stack 0
		.amdhsa_enable_private_segment 0
		.amdhsa_system_sgpr_workgroup_id_x 1
		.amdhsa_system_sgpr_workgroup_id_y 0
		.amdhsa_system_sgpr_workgroup_id_z 0
		.amdhsa_system_sgpr_workgroup_info 0
		.amdhsa_system_vgpr_workitem_id 0
		.amdhsa_next_free_vgpr 128
		.amdhsa_next_free_sgpr 96
		.amdhsa_accum_offset 128
		.amdhsa_reserve_vcc 1
		.amdhsa_float_round_mode_32 0
		.amdhsa_float_round_mode_16_64 0
		.amdhsa_float_denorm_mode_32 3
		.amdhsa_float_denorm_mode_16_64 3
		.amdhsa_dx10_clamp 1
		.amdhsa_ieee_mode 1
		.amdhsa_fp16_overflow 0
		.amdhsa_tg_split 0
		.amdhsa_exception_fp_ieee_invalid_op 0
		.amdhsa_exception_fp_denorm_src 0
		.amdhsa_exception_fp_ieee_div_zero 0
		.amdhsa_exception_fp_ieee_overflow 0
		.amdhsa_exception_fp_ieee_underflow 0
		.amdhsa_exception_fp_ieee_inexact 0
		.amdhsa_exception_int_div_zero 0
	.end_amdhsa_kernel

_Z8k_layer2PKhPKfPK15HIP_vector_typeIjLj4EEPKjS2_PKDF16_S2_Pf:
	s_lshl_b32 s3, s2, 2
	s_and_b32 s3, s3, 28
	s_and_b32 s12, s2, 0xffffffe0
	s_or_b32 s3, s3, s12
	s_bfe_u32 s12, s2, 0x20003
	s_or_b32 s3, s3, s12
	s_load_dwordx8 s[4:11], s[0:1], 0x0
	s_cmpk_eq_i32 s2, 0x3ef
	s_movk_i32 s12, 0x3f7
	s_cselect_b32 s12, s12, 0x3fb
	s_cmpk_gt_i32 s3, 0x3fc
	s_cselect_b32 s12, s12, s3
	v_lshrrev_b32_e32 v80, 3, v0
	v_lshl_or_b32 v6, s12, 5, v80
	v_ashrrev_i32_e32 v7, 31, v6
	v_or_b32_e32 v83, 0x200, v0
	v_or_b32_e32 v82, 0x300, v0
	s_waitcnt lgkmcnt(0)
	v_lshl_add_u64 v[2:3], v[6:7], 4, s[8:9]
	v_lshlrev_b32_e32 v14, 2, v0
	v_or_b32_e32 v84, 0x100, v0
	v_lshlrev_b32_e32 v7, 2, v83
	v_min_u32_e32 v8, 0x3fc, v82
	global_load_dwordx4 v[2:5], v[2:3], off
	v_lshlrev_b32_e32 v1, 2, v84
	v_lshlrev_b32_e32 v8, 2, v8
	global_load_dword v15, v14, s[6:7]
	global_load_dword v16, v1, s[6:7]
	global_load_dword v17, v7, s[6:7]
	global_load_dword v18, v8, s[6:7]
	s_movk_i32 s13, 0x188
	v_mad_u64_u32 v[6:7], s[8:9], s12, 17, v[6:7]
	v_min_i32_e32 v1, 0xc350, v6
	v_mov_b32_e32 v10, 0xc350
	v_cmp_gt_u32_e32 vcc, s13, v0
	v_lshlrev_b32_e32 v81, 4, v0
	v_and_b32_e32 v60, 0x70, v81
	v_cndmask_b32_e32 v6, v10, v1, vcc
	v_mov_b32_e32 v61, 0
	v_ashrrev_i32_e32 v7, 31, v6
	s_mul_i32 s3, s12, 49
	v_lshl_add_u64 v[8:9], s[4:5], 0, v[60:61]
	v_lshlrev_b64 v[6:7], 7, v[6:7]
	v_lshrrev_b32_e32 v1, 3, v84
	v_lshl_add_u64 v[38:39], v[8:9], 0, v[6:7]
	s_movk_i32 s8, 0x88
	v_add_u32_e32 v6, s3, v1
	v_min_i32_e32 v6, 0xc350, v6
	v_cmp_gt_u32_e32 vcc, s8, v0
	s_ashr_i32 s13, s12, 31
	s_lshl_b64 s[8:9], s[12:13], 2
	v_cndmask_b32_e32 v6, v10, v6, vcc
	v_ashrrev_i32_e32 v7, 31, v6
	v_lshlrev_b64 v[6:7], 7, v[6:7]
	v_lshl_add_u64 v[40:41], v[8:9], 0, v[6:7]
	global_load_dwordx4 v[10:13], v[38:39], off
	global_load_dwordx4 v[6:9], v[40:41], off
	s_add_u32 s8, s6, s8
	s_addc_u32 s9, s7, s9
	s_load_dword s18, s[8:9], 0x0
	s_load_dwordx4 s[12:15], s[0:1], 0x28
	s_load_dwordx2 s[6:7], s[0:1], 0x38
	v_cmp_gt_u32_e32 vcc, 64, v0
	s_waitcnt vmcnt(4)
	ds_write2st64_b32 v14, v15, v16 offset0:136 offset1:140
	v_and_b32_e32 v105, 7, v0
	v_sub_co_u32_e64 v106, s[22:23], v105, v3
	v_add_u32_e32 v107, v2, v105
	v_add_u32_e32 v106, v106, v4
	v_cndmask_b32_e64 v106, v106, v107, s[22:23]
	v_mov_b32_e32 v107, 0
	v_lshl_add_u64 v[106:107], v[106:107], 2, s[10:11]
	global_load_dword v104, v[106:107], off
	s_waitcnt vmcnt(3)
	ds_write2st64_b32 v14, v17, v18 offset0:144 offset1:148
	s_and_saveexec_b64 s[8:9], vcc
	s_cbranch_execz .LBB3_4
	v_cmp_gt_u32_e32 vcc, 49, v0
	v_mov_b32_e32 v15, 1.0
	s_and_saveexec_b64 s[16:17], vcc
	s_cbranch_execz .LBB3_3
	s_load_dwordx2 s[0:1], s[0:1], 0x20
	v_add_u32_e32 v15, s3, v0
	v_min_i32_e32 v16, 0xc34f, v15
	v_ashrrev_i32_e32 v17, 31, v16
	s_waitcnt lgkmcnt(0)
	v_lshl_add_u64 v[16:17], v[16:17], 2, s[0:1]
	global_load_dword v16, v[16:17], off
	s_mov_b32 s0, 0xc350
	v_cmp_gt_i32_e32 vcc, s0, v15
	s_waitcnt vmcnt(0)
	s_nop 0
	v_cndmask_b32_e32 v15, 1.0, v16, vcc

.LBB3_4:
	s_or_b64 exec, exec, s[8:9]
	v_and_b32_e32 v47, 7, v0
	v_lshlrev_b32_e32 v49, 2, v47
	v_mul_u32_u24_e32 v14, 0x220, v80
	s_waitcnt vmcnt(2)
	v_cvt_f32_ubyte0_e32 v15, v10
	v_cvt_f32_ubyte1_e32 v16, v10
	v_or_b32_e32 v14, v49, v14
	s_waitcnt lgkmcnt(0)
	v_mul_f32_e32 v15, s18, v15
	v_mul_f32_e32 v16, s18, v16
	ds_write2_b32 v14, v15, v16 offset1:8
	v_cvt_f32_ubyte2_e32 v15, v10
	v_cvt_f32_ubyte3_e32 v10, v10
	v_mul_f32_e32 v15, s18, v15
	v_mul_f32_e32 v10, s18, v10
	ds_write2_b32 v14, v15, v10 offset0:16 offset1:24
	v_cvt_f32_ubyte0_e32 v10, v11
	v_cvt_f32_ubyte1_e32 v15, v11
	v_mul_f32_e32 v10, s18, v10
	v_mul_f32_e32 v15, s18, v15
	ds_write2_b32 v14, v10, v15 offset0:32 offset1:40
	v_cvt_f32_ubyte2_e32 v10, v11
	v_cvt_f32_ubyte3_e32 v11, v11
	v_mul_f32_e32 v10, s18, v10
	v_mul_f32_e32 v11, s18, v11
	ds_write2_b32 v14, v10, v11 offset0:48 offset1:56
	v_cvt_f32_ubyte0_e32 v10, v12
	v_cvt_f32_ubyte1_e32 v11, v12
	v_mul_f32_e32 v10, s18, v10
	v_mul_f32_e32 v11, s18, v11
	ds_write2_b32 v14, v10, v11 offset0:64 offset1:72
	v_cvt_f32_ubyte2_e32 v10, v12
	v_cvt_f32_ubyte3_e32 v11, v12
	v_mul_f32_e32 v10, s18, v10
	v_mul_f32_e32 v11, s18, v11
	ds_write2_b32 v14, v10, v11 offset0:80 offset1:88
	v_cvt_f32_ubyte0_e32 v10, v13
	v_cvt_f32_ubyte1_e32 v11, v13
	v_mul_f32_e32 v10, s18, v10
	v_mul_f32_e32 v11, s18, v11
	ds_write2_b32 v14, v10, v11 offset0:96 offset1:104
	v_cvt_f32_ubyte2_e32 v10, v13
	v_cvt_f32_ubyte3_e32 v11, v13
	v_mul_f32_e32 v10, s18, v10
	v_mul_f32_e32 v11, s18, v11
	ds_write2_b32 v14, v10, v11 offset0:112 offset1:120
	v_mul_u32_u24_e32 v10, 0x220, v1
	s_waitcnt vmcnt(1)
	v_cvt_f32_ubyte0_e32 v11, v6
	v_cvt_f32_ubyte1_e32 v12, v6
	v_or_b32_e32 v10, v49, v10
	v_mul_f32_e32 v11, s18, v11
	v_mul_f32_e32 v12, s18, v12
	ds_write2_b32 v10, v11, v12 offset1:8
	v_cvt_f32_ubyte2_e32 v11, v6
	v_cvt_f32_ubyte3_e32 v6, v6
	v_mul_f32_e32 v11, s18, v11
	v_mul_f32_e32 v6, s18, v6
	ds_write2_b32 v10, v11, v6 offset0:16 offset1:24
	v_cvt_f32_ubyte0_e32 v6, v7
	v_cvt_f32_ubyte1_e32 v11, v7
	v_mul_f32_e32 v6, s18, v6
	v_mul_f32_e32 v11, s18, v11
	ds_write2_b32 v10, v6, v11 offset0:32 offset1:40
	v_cvt_f32_ubyte2_e32 v6, v7
	v_cvt_f32_ubyte3_e32 v7, v7
	v_mul_f32_e32 v6, s18, v6
	v_mul_f32_e32 v7, s18, v7
	ds_write2_b32 v10, v6, v7 offset0:48 offset1:56
	v_cvt_f32_ubyte0_e32 v6, v8
	v_cvt_f32_ubyte1_e32 v7, v8
	v_mul_f32_e32 v6, s18, v6
	v_mul_f32_e32 v7, s18, v7
	ds_write2_b32 v10, v6, v7 offset0:64 offset1:72
	v_cvt_f32_ubyte2_e32 v6, v8
	v_cvt_f32_ubyte3_e32 v7, v8
	v_mul_f32_e32 v6, s18, v6
	v_mul_f32_e32 v7, s18, v7
	ds_write2_b32 v10, v6, v7 offset0:80 offset1:88
	v_cvt_f32_ubyte0_e32 v6, v9
	v_cvt_f32_ubyte1_e32 v7, v9
	v_mul_f32_e32 v6, s18, v6
	v_mul_f32_e32 v7, s18, v7
	ds_write2_b32 v10, v6, v7 offset0:96 offset1:104
	v_cvt_f32_ubyte2_e32 v6, v9
	v_cvt_f32_ubyte3_e32 v7, v9
	v_mul_f32_e32 v6, s18, v6
	v_mul_f32_e32 v7, s18, v7
	ds_write2_b32 v10, v6, v7 offset0:112 offset1:120
	s_waitcnt lgkmcnt(0)
	s_barrier
	s_setprio 2
	v_mov_b32_e32 v65, 0
	v_mbcnt_lo_u32_b32 v7, -1, 0
	v_add_u32_e32 v5, v5, v3
	v_mbcnt_hi_u32_b32 v61, -1, v7
	v_mov_b32_e32 v51, 0x100c350
	v_lshlrev_b32_e32 v15, 2, v61
	v_cmp_lt_u32_e32 vcc, v47, v5
	v_and_b32_e32 v55, 0x1e0, v15
	v_add_u32_e32 v14, 7, v5
	v_mov_b32_e32 v67, v65
	v_mov_b32_e32 v66, v65
	v_mov_b32_e32 v69, v65
	v_mov_b32_e32 v68, v65
	v_mov_b32_e32 v71, v65
	v_mov_b32_e32 v70, v65
	v_mov_b32_e32 v73, v65
	v_mov_b32_e32 v72, v65
	v_mov_b32_e32 v75, v65
	v_mov_b32_e32 v74, v65
	v_mov_b32_e32 v77, v65
	v_mov_b32_e32 v76, v65
	v_mov_b32_e32 v79, v65
	v_mov_b32_e32 v64, v65
	v_mov_b32_e32 v78, v65
	s_waitcnt vmcnt(0)
	v_cndmask_b32_e32 v95, v51, v104, vcc
	ds_bpermute_b32 v9, v55, v95
	ds_bpermute_b32 v8, v55, v95 offset:4
	ds_bpermute_b32 v7, v55, v95 offset:8
	ds_bpermute_b32 v6, v55, v95 offset:12
	v_cmp_lt_u32_e32 vcc, 7, v14
	s_waitcnt lgkmcnt(3)
	v_lshrrev_b32_e32 v98, 16, v9
	s_and_saveexec_b64 s[8:9], vcc
	s_cbranch_execz .LBB3_24
	v_lshlrev_b32_e32 v42, 4, v47
	v_mov_b32_e32 v43, 0
	s_waitcnt lgkmcnt(0)
	v_and_b32_e32 v29, 0xffff, v6
	v_lshl_add_u64 v[44:45], s[4:5], 0, v[42:43]
	v_and_b32_e32 v28, 0xffff, v7
	v_lshlrev_b32_e32 v42, 7, v29
	v_lshl_add_u64 v[16:17], v[44:45], 0, v[42:43]
	v_lshlrev_b32_e32 v42, 7, v28
	v_and_b32_e32 v27, 0xffff, v8
	v_lshl_add_u64 v[18:19], v[44:45], 0, v[42:43]
	v_or_b32_e32 v34, 8, v47
	v_and_b32_e32 v26, 0xffff, v9
	global_load_dwordx4 v[6:9], v[16:17], off
	global_load_dwordx4 v[10:13], v[18:19], off
	v_lshlrev_b32_e32 v42, 7, v27
	v_sub_co_u32_e32 v19, vcc, v34, v3
	v_lshl_add_u64 v[16:17], v[44:45], 0, v[42:43]
	v_lshlrev_b32_e32 v42, 7, v26
	v_add_u32_e32 v18, v2, v34
	v_add_u32_e32 v19, v19, v4
	v_lshl_add_u64 v[22:23], v[44:45], 0, v[42:43]
	v_cndmask_b32_e32 v42, v19, v18, vcc
	v_lshl_add_u64 v[24:25], v[42:43], 2, s[10:11]
	global_load_dword v35, v[24:25], off
	global_load_dwordx4 v[18:21], v[16:17], off
	global_load_dwordx4 v[30:33], v[22:23], off
	s_mov_b32 s19, 0x539782a
	v_lshrrev_b32_e32 v88, 3, v14
	v_mul_hi_u32 v14, v26, s19
	v_or_b32_e32 v93, 28, v15
	v_mul_hi_u32 v15, v27, s19
	v_mul_hi_u32 v16, v28, s19
	v_mul_hi_u32 v17, v29, s19
	v_lshlrev_b32_e32 v14, 2, v14
	v_lshlrev_b32_e32 v15, 2, v15
	v_lshlrev_b32_e32 v16, 2, v16
	v_lshlrev_b32_e32 v17, 2, v17
	ds_read_b32 v56, v14 offset:34816
	ds_read_b32 v57, v15 offset:34816
	ds_read_b32 v50, v16 offset:34816
	ds_read_b32 v46, v17 offset:34816
	v_cmp_lt_u32_e64 s[0:1], v34, v5
	v_or_b32_e32 v85, 4, v55
	v_or_b32_e32 v86, 8, v55
	v_or_b32_e32 v87, 12, v55
	v_sub_u32_e32 v89, v4, v3
	v_cmp_eq_u32_e32 vcc, 0, v47
	v_and_b32_e32 v4, 56, v61
	v_or_b32_e32 v90, 16, v55
	v_or_b32_e32 v91, 20, v55
	v_or_b32_e32 v92, 24, v55
	v_or_b32_e32 v94, 16, v47
	s_mov_b64 s[16:17], 0
	s_mov_b32 s20, 0x1000000
	v_mov_b32_e32 v78, v43
	v_mov_b32_e32 v79, v43
	v_mov_b32_e32 v76, v43
	v_mov_b32_e32 v77, v43
	v_mov_b32_e32 v74, v43
	v_mov_b32_e32 v75, v43
	v_mov_b32_e32 v72, v43
	v_mov_b32_e32 v73, v43
	v_mov_b32_e32 v70, v43
	v_mov_b32_e32 v71, v43
	v_mov_b32_e32 v68, v43
	v_mov_b32_e32 v69, v43
	v_mov_b32_e32 v66, v43
	v_mov_b32_e32 v67, v43
	v_mov_b32_e32 v64, v43
	v_mov_b32_e32 v65, v43
	s_waitcnt vmcnt(2)
	v_cndmask_b32_e64 v96, v51, v35, s[0:1]
	s_branch .LBB3_7

.LBB3_26:
	s_or_b64 exec, exec, s[0:1]
	v_and_b32_e32 v62, 63, v0
	v_bfe_u32 v63, v0, 5, 1
	v_lshrrev_b32_e32 v64, 6, v0
	v_and_b32_e32 v65, 31, v0
	s_setprio 0
	s_waitcnt vmcnt(1)
	v_lshlrev_b32_e32 v10, 4, v62
	v_lshl_or_b32 v10, v64, 13, v10
	v_mov_b32_e32 v11, 0
	v_lshl_add_u64 v[12:13], s[12:13], 0, v[10:11]
	s_movk_i32 s0, 0x1000
	s_waitcnt lgkmcnt(0)
	global_load_dwordx4 v[6:9], v[38:39], off
	global_load_dwordx4 v[2:5], v[40:41], off
	global_load_dwordx4 v[16:19], v10, s[12:13]
	global_load_dwordx4 v[56:59], v10, s[12:13] offset:1024
	global_load_dwordx4 v[52:55], v10, s[12:13] offset:2048
	global_load_dwordx4 v[48:51], v10, s[12:13] offset:3072
	v_add_co_u32_e32 v10, vcc, s0, v12
	v_lshrrev_b32_e32 v23, 4, v0
	s_nop 0
	v_addc_co_u32_e32 v11, vcc, 0, v13, vcc
	global_load_dwordx4 v[44:47], v[10:11], off
	global_load_dwordx4 v[40:43], v[10:11], off offset:1024
	global_load_dwordx4 v[36:39], v[10:11], off offset:2048
	global_load_dwordx4 v[32:35], v[10:11], off offset:3072
	v_lshlrev_b32_e32 v10, 1, v0
	v_and_b32_e32 v11, 28, v10
	v_lshlrev_b32_e32 v10, 8, v0
	v_and_b32_e32 v21, 0x100, v10
	v_mul_u32_u24_e32 v10, 0x220, v23
	v_or_b32_e32 v10, v11, v10
	v_lshlrev_b32_e32 v0, 2, v23
	v_add_u32_e32 v26, v10, v21
	s_barrier
	ds_read_b32 v0, v0 offset:38912
	ds_read2_b32 v[12:13], v26 offset1:8
	ds_read2_b32 v[14:15], v26 offset0:16 offset1:24
	v_lshrrev_b32_e32 v66, 4, v84
	v_lshrrev_b32_e32 v67, 4, v83
	v_lshrrev_b32_e32 v68, 4, v82
	v_lshlrev_b32_e32 v10, 2, v66
	v_lshlrev_b32_e32 v22, 2, v67
	v_lshlrev_b32_e32 v24, 2, v68
	ds_read_b32 v20, v10 offset:38912
	ds_read_b32 v22, v22 offset:38912
	ds_read_b32 v10, v24 offset:38912
	ds_read2_b32 v[24:25], v26 offset0:32 offset1:40
	s_waitcnt lgkmcnt(5)
	v_fma_mixlo_f16 v69, v0, v12, 0
	v_mov_b32_e32 v12, v13
	s_waitcnt lgkmcnt(4)
	v_mov_b32_e32 v13, v14
	v_mul_f32_e32 v12, v0, v12
	v_mul_f32_e32 v13, v0, v13
	v_cvt_pk_f16_f32 v70, v12, v13
	v_mov_b32_e32 v12, v15
	s_waitcnt lgkmcnt(0)
	v_mov_b32_e32 v13, v24
	v_mul_f32_e32 v12, v0, v12
	v_mul_f32_e32 v13, v0, v13
	v_cvt_pk_f16_f32 v71, v12, v13
	v_mul_u32_u24_e32 v13, 0x220, v66
	ds_read2_b32 v[26:27], v26 offset0:48 offset1:56
	v_or_b32_e32 v13, v11, v13
	v_add_u32_e32 v28, v13, v21
	ds_read2_b32 v[14:15], v28 offset1:8
	v_mov_b32_e32 v12, v25
	s_waitcnt lgkmcnt(1)
	v_mov_b32_e32 v13, v26
	ds_read2_b32 v[24:25], v28 offset0:16 offset1:24
	v_mul_f32_e32 v12, v0, v12
	v_mul_f32_e32 v13, v0, v13
	v_cvt_pk_f16_f32 v26, v12, v13
	s_waitcnt lgkmcnt(1)
	v_fma_mixlo_f16 v72, v20, v14, 0
	v_mov_b32_e32 v12, v15
	ds_read2_b32 v[14:15], v28 offset0:32 offset1:40
	s_waitcnt lgkmcnt(1)
	v_mov_b32_e32 v13, v24
	v_mul_f32_e32 v12, v20, v12
	v_mul_f32_e32 v13, v20, v13
	v_cvt_pk_f16_f32 v73, v12, v13
	v_mov_b32_e32 v12, v25
	s_waitcnt lgkmcnt(0)
	v_mov_b32_e32 v13, v14
	v_mul_f32_e32 v12, v20, v12
	v_mul_f32_e32 v13, v20, v13
	v_cvt_pk_f16_f32 v74, v12, v13
	v_mul_u32_u24_e32 v13, 0x220, v67
	ds_read2_b32 v[24:25], v28 offset0:48 offset1:56
	v_or_b32_e32 v13, v11, v13
	v_add_u32_e32 v30, v13, v21
	v_mov_b32_e32 v12, v15
	ds_read2_b32 v[14:15], v30 offset1:8
	s_waitcnt lgkmcnt(1)
	v_mov_b32_e32 v13, v24
	ds_read2_b32 v[28:29], v30 offset0:16 offset1:24
	v_mul_f32_e32 v12, v20, v12
	v_mul_f32_e32 v13, v20, v13
	v_cvt_pk_f16_f32 v24, v12, v13
	s_waitcnt lgkmcnt(1)
	v_fma_mixlo_f16 v75, v22, v14, 0
	v_mov_b32_e32 v12, v15
	ds_read2_b32 v[14:15], v30 offset0:32 offset1:40
	s_waitcnt lgkmcnt(1)
	v_mov_b32_e32 v13, v28
	v_mul_f32_e32 v12, v22, v12
	v_mul_f32_e32 v13, v22, v13
	v_cvt_pk_f16_f32 v76, v12, v13
	v_mov_b32_e32 v12, v29
	s_waitcnt lgkmcnt(0)
	v_mov_b32_e32 v13, v14
	v_mul_f32_e32 v12, v22, v12
	v_mul_f32_e32 v13, v22, v13
	v_cvt_pk_f16_f32 v77, v12, v13
	v_mul_u32_u24_e32 v13, 0x220, v68
	ds_read2_b32 v[28:29], v30 offset0:48 offset1:56
	v_or_b32_e32 v11, v11, v13
	v_add_u32_e32 v11, v11, v21
	v_mov_b32_e32 v12, v15
	ds_read2_b32 v[14:15], v11 offset1:8
	ds_read2_b32 v[30:31], v11 offset0:16 offset1:24
	s_waitcnt lgkmcnt(2)
	v_mov_b32_e32 v13, v28
	v_mul_f32_e32 v12, v22, v12
	v_mul_f32_e32 v13, v22, v13
	v_cvt_pk_f16_f32 v21, v12, v13
	s_waitcnt lgkmcnt(1)
	v_fma_mixlo_f16 v28, v10, v14, 0
	v_mov_b32_e32 v12, v15
	s_waitcnt lgkmcnt(0)
	v_mov_b32_e32 v13, v30
	ds_read2_b32 v[14:15], v11 offset0:32 offset1:40
	v_mul_f32_e32 v12, v10, v12
	v_mul_f32_e32 v13, v10, v13
	v_cvt_pk_f16_f32 v78, v12, v13
	v_mov_b32_e32 v12, v31
	ds_read2_b32 v[30:31], v11 offset0:48 offset1:56
	s_waitcnt lgkmcnt(1)
	v_mov_b32_e32 v13, v14
	v_mul_f32_e32 v12, v10, v12
	v_mul_f32_e32 v13, v10, v13
	v_cvt_pk_f16_f32 v11, v12, v13
	v_mov_b32_e32 v12, v15
	s_waitcnt lgkmcnt(0)
	v_mov_b32_e32 v13, v30
	v_mul_f32_e32 v12, v10, v12
	v_mul_f32_e32 v13, v10, v13
	v_and_b32_e32 v79, 0xf0, v81
	v_lshrrev_b32_e32 v15, 16, v26
	s_movk_i32 s0, 0x110
	v_cvt_pk_f16_f32 v30, v12, v13
	v_pack_b32_f16 v12, v69, v70
	v_alignbit_b32 v13, v71, v70, 16
	v_alignbit_b32 v14, v26, v71, 16
	v_fma_mixhi_f16 v15, v0, v27, 0
	v_mad_u32_u24 v0, v23, s0, v79
	s_barrier
	ds_write_b128 v0, v[12:15]
	v_lshrrev_b32_e32 v15, 16, v24
	v_pack_b32_f16 v12, v72, v73
	v_alignbit_b32 v13, v74, v73, 16
	v_alignbit_b32 v14, v24, v74, 16
	v_fma_mixhi_f16 v15, v20, v25, 0
	v_mad_u32_u24 v0, v66, s0, v79
	ds_write_b128 v0, v[12:15]
	v_lshrrev_b32_e32 v15, 16, v21
	v_pack_b32_f16 v12, v75, v76
	v_alignbit_b32 v13, v77, v76, 16
	v_alignbit_b32 v14, v21, v77, 16
	v_fma_mixhi_f16 v15, v22, v29, 0
	v_mad_u32_u24 v0, v67, s0, v79
	ds_write_b128 v0, v[12:15]
	v_lshlrev_b32_e32 v0, 2, v80
	ds_read_b32 v0, v0 offset:38912
	v_lshrrev_b32_e32 v15, 16, v30
	v_fma_mixhi_f16 v15, v10, v31, 0
	v_lshlrev_b32_e32 v10, 2, v1
	ds_read_b32 v24, v10 offset:38912
	s_waitcnt lgkmcnt(1)
	v_div_scale_f32 v10, s[4:5], v0, v0, s18
	v_alignbit_b32 v13, v11, v78, 16
	v_alignbit_b32 v14, v30, v11, 16
	v_rcp_f32_e32 v11, v10
	v_pack_b32_f16 v12, v28, v78
	v_mad_u32_u24 v20, v68, s0, v79
	ds_write_b128 v20, v[12:15]
	v_fma_f32 v12, -v10, v11, 1.0
	v_fmac_f32_e32 v11, v12, v11
	v_div_scale_f32 v12, vcc, s18, v0, s18
	v_mul_f32_e32 v13, v12, v11
	v_fma_f32 v14, -v10, v13, v12
	v_fmac_f32_e32 v13, v14, v11
	v_fma_f32 v10, -v10, v13, v12
	v_div_fmas_f32 v10, v10, v11, v13
	v_div_fixup_f32 v0, v10, v0, s18
	s_waitcnt vmcnt(9)
	v_cvt_f32_ubyte1_e32 v13, v8
	v_cvt_f32_ubyte0_e32 v12, v8
	v_mul_f32_e32 v12, v0, v12
	v_mul_f32_e32 v13, v0, v13
	v_cvt_f32_ubyte1_e32 v11, v6
	v_cvt_f32_ubyte0_e32 v10, v6
	v_cvt_pk_f16_f32 v20, v12, v13
	v_cvt_f32_ubyte3_e32 v13, v6
	v_cvt_f32_ubyte2_e32 v12, v6
	v_mul_f32_e32 v10, v0, v10
	v_mul_f32_e32 v11, v0, v11
	v_mul_f32_e32 v12, v0, v12
	v_mul_f32_e32 v13, v0, v13
	v_cvt_pk_f16_f32 v10, v10, v11
	v_cvt_pk_f16_f32 v11, v12, v13
	v_cvt_f32_ubyte3_e32 v13, v8
	v_cvt_f32_ubyte2_e32 v12, v8
	v_cvt_f32_ubyte1_e32 v15, v9
	v_cvt_f32_ubyte0_e32 v14, v9
	v_mul_f32_e32 v12, v0, v12
	v_mul_f32_e32 v13, v0, v13
	v_mul_f32_e32 v14, v0, v14
	v_mul_f32_e32 v15, v0, v15
	v_cvt_pk_f16_f32 v21, v12, v13
	v_cvt_f32_ubyte1_e32 v13, v7
	v_cvt_f32_ubyte0_e32 v12, v7
	v_cvt_pk_f16_f32 v22, v14, v15
	v_cvt_f32_ubyte3_e32 v15, v7
	v_cvt_f32_ubyte2_e32 v14, v7
	v_mul_f32_e32 v12, v0, v12
	v_mul_f32_e32 v13, v0, v13
	v_mul_f32_e32 v6, v0, v14
	v_mul_f32_e32 v7, v0, v15
	v_cvt_pk_f16_f32 v12, v12, v13
	v_cvt_pk_f16_f32 v13, v6, v7
	v_cvt_f32_ubyte3_e32 v7, v9
	v_cvt_f32_ubyte2_e32 v6, v9
	v_mul_f32_e32 v6, v0, v6
	v_mul_f32_e32 v7, v0, v7
	s_waitcnt lgkmcnt(1)
	v_div_scale_f32 v0, s[4:5], v24, v24, s18
	v_cvt_pk_f16_f32 v23, v6, v7
	v_rcp_f32_e32 v6, v0
	v_lshlrev_b32_e32 v25, 1, v60
	v_mad_u32_u24 v7, v80, s0, v25
	ds_write_b128 v7, v[10:13] offset:17408
	ds_write_b128 v7, v[20:23] offset:17424
	v_fma_f32 v7, -v0, v6, 1.0
	v_fmac_f32_e32 v6, v7, v6
	v_div_scale_f32 v7, vcc, s18, v24, s18
	v_mul_f32_e32 v8, v7, v6
	v_fma_f32 v9, -v0, v8, v7
	v_fmac_f32_e32 v8, v9, v6
	v_fma_f32 v0, -v0, v8, v7
	v_div_fmas_f32 v0, v0, v6, v8
	v_div_fixup_f32 v0, v0, v24, s18
	s_waitcnt vmcnt(8)
	v_cvt_f32_ubyte1_e32 v9, v4
	v_cvt_f32_ubyte0_e32 v8, v4
	v_mul_f32_e32 v8, v0, v8
	v_mul_f32_e32 v9, v0, v9
	v_cvt_f32_ubyte1_e32 v7, v2
	v_cvt_f32_ubyte0_e32 v6, v2
	v_cvt_pk_f16_f32 v10, v8, v9
	v_cvt_f32_ubyte3_e32 v9, v2
	v_cvt_f32_ubyte2_e32 v8, v2
	v_mul_f32_e32 v6, v0, v6
	v_mul_f32_e32 v7, v0, v7
	v_mul_f32_e32 v8, v0, v8
	v_mul_f32_e32 v9, v0, v9
	v_cvt_pk_f16_f32 v6, v6, v7
	v_cvt_pk_f16_f32 v7, v8, v9
	v_cvt_f32_ubyte3_e32 v9, v4
	v_cvt_f32_ubyte2_e32 v8, v4
	v_mul_f32_e32 v8, v0, v8
	v_mul_f32_e32 v9, v0, v9
	v_cvt_pk_f16_f32 v11, v8, v9
	v_cvt_f32_ubyte1_e32 v9, v3
	v_cvt_f32_ubyte0_e32 v8, v3
	v_cvt_f32_ubyte3_e32 v15, v3
	v_cvt_f32_ubyte2_e32 v14, v3
	v_mul_f32_e32 v8, v0, v8
	v_mul_f32_e32 v9, v0, v9
	v_mul_f32_e32 v2, v0, v14
	v_mul_f32_e32 v3, v0, v15
	v_cvt_pk_f16_f32 v8, v8, v9
	v_cvt_f32_ubyte1_e32 v13, v5
	v_cvt_f32_ubyte0_e32 v12, v5
	v_cvt_pk_f16_f32 v9, v2, v3
	v_cvt_f32_ubyte3_e32 v3, v5
	v_cvt_f32_ubyte2_e32 v2, v5
	v_mul_f32_e32 v12, v0, v12
	v_mul_f32_e32 v13, v0, v13
	v_mul_f32_e32 v2, v0, v2
	v_mul_f32_e32 v3, v0, v3
	v_mad_u32_u24 v0, v1, s0, v25
	v_cvt_pk_f16_f32 v12, v12, v13
	v_cvt_pk_f16_f32 v13, v2, v3
	ds_write_b128 v0, v[6:9] offset:17408
	ds_write_b128 v0, v[10:13] offset:17424
	v_lshlrev_b32_e32 v0, 4, v63
	v_mad_u32_u24 v60, v65, s0, v0
	s_waitcnt lgkmcnt(0)
	s_barrier
	ds_read_b128 v[0:3], v60
	ds_read_b128 v[66:69], v60 offset:32
	s_waitcnt vmcnt(7) lgkmcnt(1)
	v_mfma_f32_32x32x16_f16 v[0:15], v[0:3], v[16:19], 0
	ds_read_b128 v[20:23], v60 offset:8704
	ds_read_b128 v[70:73], v60 offset:8736
	s_add_i32 s0, s3, 32
	s_mov_b32 s4, 0xc350
	s_waitcnt lgkmcnt(1)
	v_mfma_f32_32x32x16_f16 v[16:31], v[20:23], v[16:19], 0
	s_waitcnt vmcnt(6)
	v_mfma_f32_32x32x16_f16 v[0:15], v[66:69], v[56:59], v[0:15]
	s_waitcnt lgkmcnt(0)
	v_mfma_f32_32x32x16_f16 v[16:31], v[70:73], v[56:59], v[16:31]
	ds_read_b128 v[56:59], v60 offset:64
	ds_read_b128 v[66:69], v60 offset:96
	s_waitcnt vmcnt(5) lgkmcnt(1)
	v_mfma_f32_32x32x16_f16 v[0:15], v[56:59], v[52:55], v[0:15]
	ds_read_b128 v[56:59], v60 offset:8768
	ds_read_b128 v[70:73], v60 offset:8800
	s_waitcnt lgkmcnt(1)
	v_mfma_f32_32x32x16_f16 v[16:31], v[56:59], v[52:55], v[16:31]
	s_waitcnt vmcnt(4)
	v_mfma_f32_32x32x16_f16 v[0:15], v[66:69], v[48:51], v[0:15]
	s_waitcnt lgkmcnt(0)
	v_mfma_f32_32x32x16_f16 v[16:31], v[70:73], v[48:51], v[16:31]
	ds_read_b128 v[48:51], v60 offset:128
	ds_read_b128 v[52:55], v60 offset:160
	s_waitcnt vmcnt(3) lgkmcnt(1)
	v_mfma_f32_32x32x16_f16 v[0:15], v[48:51], v[44:47], v[0:15]
	ds_read_b128 v[48:51], v60 offset:8832
	ds_read_b128 v[56:59], v60 offset:8864
	s_waitcnt lgkmcnt(1)
	v_mfma_f32_32x32x16_f16 v[16:31], v[48:51], v[44:47], v[16:31]
	s_waitcnt vmcnt(2)
	v_mfma_f32_32x32x16_f16 v[0:15], v[52:55], v[40:43], v[0:15]
	s_waitcnt lgkmcnt(0)
	v_mfma_f32_32x32x16_f16 v[16:31], v[56:59], v[40:43], v[16:31]
	ds_read_b128 v[40:43], v60 offset:192
	ds_read_b128 v[44:47], v60 offset:224
	s_waitcnt vmcnt(1) lgkmcnt(1)
	v_mfma_f32_32x32x16_f16 v[0:15], v[40:43], v[36:39], v[0:15]
	ds_read_b128 v[40:43], v60 offset:8896
	ds_read_b128 v[48:51], v60 offset:8928
	s_waitcnt lgkmcnt(1)
	v_mfma_f32_32x32x16_f16 v[16:31], v[40:43], v[36:39], v[16:31]
	v_lshl_or_b32 v36, v64, 5, v65
	v_lshlrev_b32_e32 v37, 2, v36
	global_load_dword v37, v37, s[14:15]
	s_waitcnt vmcnt(1)
	v_mfma_f32_32x32x16_f16 v[0:15], v[44:47], v[32:35], v[0:15]
	v_bfrev_b32_e32 v45, 1
	s_waitcnt lgkmcnt(0)
	v_mfma_f32_32x32x16_f16 v[16:31], v[48:51], v[32:35], v[16:31]
	s_waitcnt vmcnt(0)
	s_add_i32 s5, s3, 49
	s_cmp_le_u32 s5, s4
	s_cbranch_scc1 .Lfast_sum_l2
	s_nop 7
	v_add_f32_e32 v1, v37, v1
	s_nop 1
	v_add_f32_e32 v26, v37, v0
	v_mul_u32_u24_e32 v0, 0x440, v63
	v_lshl_add_u32 v0, v36, 1, v0
	ds_read_u16 v27, v0 offset:17408
	ds_read_u16 v28, v0 offset:17680
	ds_read_u16 v29, v0 offset:17952
	ds_read_u16 v30, v0 offset:18224
	ds_read_u16 v31, v0 offset:19584
	ds_read_u16 v32, v0 offset:19856
	ds_read_u16 v33, v0 offset:20128
	ds_read_u16 v34, v0 offset:20400
	ds_read_u16 v35, v0 offset:26112
	ds_read_u16 v38, v0 offset:26384
	ds_read_u16 v39, v0 offset:26656
	ds_read_u16 v40, v0 offset:26928
	ds_read_u16 v41, v0 offset:28288
	ds_read_u16 v42, v0 offset:28560
	ds_read_u16 v43, v0 offset:28832
	ds_read_u16 v44, v0 offset:29104
	s_waitcnt lgkmcnt(14)
	v_cvt_f32_f16_e32 v27, v27
	s_waitcnt lgkmcnt(7)
	v_cvt_f32_f16_e32 v35, v35
	v_add_f32_e32 v16, v37, v16
	v_lshlrev_b32_e32 v25, 2, v63
	v_add_f32_e32 v26, v26, v27
	v_add_f32_e32 v16, v16, v35
	v_max_f32_e32 v26, 0, v26
	v_max_f32_e32 v27, 0, v16
	v_add_u32_e32 v16, s3, v25
	v_add_f32_e32 v26, 0, v26
	v_cmp_gt_i32_e32 vcc, s4, v16
	v_add_u32_e32 v35, s0, v25
	v_add_f32_e32 v17, v37, v17
	v_cndmask_b32_e32 v26, 0, v26, vcc
	v_cmp_gt_i32_e32 vcc, s4, v35
	s_waitcnt lgkmcnt(6)
	v_cvt_f32_f16_e32 v35, v38
	v_add_f32_e32 v2, v37, v2
	v_cndmask_b32_e32 v27, v45, v27, vcc
	v_add_f32_e32 v26, v26, v27
	v_cvt_f32_f16_e32 v27, v28
	v_or_b32_e32 v28, 1, v25
	v_add_f32_e32 v17, v17, v35
	v_max_f32_e32 v17, 0, v17
	v_add_f32_e32 v1, v1, v27
	v_max_f32_e32 v1, 0, v1
	v_add_u32_e32 v27, s3, v28
	v_add_f32_e32 v1, v26, v1
	v_cmp_gt_i32_e32 vcc, s4, v27
	s_waitcnt lgkmcnt(5)
	v_cvt_f32_f16_e32 v27, v39
	v_add_f32_e32 v3, v37, v3
	v_cndmask_b32_e32 v1, v26, v1, vcc
	v_add_u32_e32 v26, s0, v28
	v_add_f32_e32 v17, v17, v1
	v_cmp_gt_i32_e32 vcc, s4, v26
	v_or_b32_e32 v26, 2, v25
	v_add_f32_e32 v4, v37, v4
	v_cndmask_b32_e32 v1, v1, v17, vcc
	v_cvt_f32_f16_e32 v17, v29
	v_add_f32_e32 v8, v37, v8
	v_add_f32_e32 v2, v2, v17
	v_max_f32_e32 v2, 0, v2
	v_add_f32_e32 v17, v37, v18
	v_add_u32_e32 v18, s3, v26
	v_add_f32_e32 v2, v1, v2
	v_cmp_gt_i32_e32 vcc, s4, v18
	v_add_f32_e32 v17, v17, v27
	s_waitcnt lgkmcnt(4)
	v_cvt_f32_f16_e32 v18, v40
	v_cndmask_b32_e32 v1, v1, v2, vcc
	v_add_u32_e32 v2, s0, v26
	v_cmp_gt_i32_e32 vcc, s4, v2
	v_cvt_f32_f16_e32 v2, v30
	v_max_f32_e32 v17, 0, v17
	v_add_f32_e32 v17, v17, v1
	v_cndmask_b32_e32 v1, v1, v17, vcc
	v_or_b32_e32 v17, 3, v25
	v_add_f32_e32 v2, v3, v2
	v_add_f32_e32 v3, v37, v19
	v_max_f32_e32 v2, 0, v2
	v_add_f32_e32 v3, v3, v18
	v_add_u32_e32 v18, s3, v17
	v_add_f32_e32 v2, v1, v2
	v_cmp_gt_i32_e32 vcc, s4, v18
	v_max_f32_e32 v3, 0, v3
	v_or_b32_e32 v19, 16, v25
	v_cndmask_b32_e32 v1, v1, v2, vcc
	v_add_u32_e32 v2, s0, v17
	v_cmp_gt_i32_e32 vcc, s4, v2
	v_cvt_f32_f16_e32 v2, v31
	s_waitcnt lgkmcnt(3)
	v_cvt_f32_f16_e32 v17, v41
	v_add_f32_e32 v3, v3, v1
	v_cndmask_b32_e32 v1, v1, v3, vcc
	v_or_b32_e32 v3, 8, v25
	v_add_f32_e32 v2, v4, v2
	v_add_f32_e32 v4, v37, v20
	v_max_f32_e32 v2, 0, v2
	v_add_f32_e32 v4, v4, v17
	v_add_u32_e32 v17, s3, v3
	v_add_f32_e32 v2, v1, v2
	v_cmp_gt_i32_e32 vcc, s4, v17
	v_max_f32_e32 v4, 0, v4
	s_nop 0
	v_cndmask_b32_e32 v1, v1, v2, vcc
	v_add_u32_e32 v2, s0, v3
	v_cmp_gt_i32_e32 vcc, s4, v2
	v_cvt_f32_f16_e32 v2, v32
	v_add_f32_e32 v3, v4, v1
	v_add_f32_e32 v4, v37, v5
	s_waitcnt lgkmcnt(2)
	v_cvt_f32_f16_e32 v5, v42
	v_cndmask_b32_e32 v1, v1, v3, vcc
	v_or_b32_e32 v3, 9, v25
	v_add_f32_e32 v2, v4, v2
	v_add_f32_e32 v4, v37, v21
	v_max_f32_e32 v2, 0, v2
	v_add_f32_e32 v4, v4, v5
	v_add_u32_e32 v5, s3, v3
	v_add_f32_e32 v2, v1, v2
	v_cmp_gt_i32_e32 vcc, s4, v5
	s_waitcnt lgkmcnt(1)
	v_cvt_f32_f16_e32 v5, v43
	v_max_f32_e32 v4, 0, v4
	v_cndmask_b32_e32 v1, v1, v2, vcc
	v_add_u32_e32 v2, s0, v3
	v_cmp_gt_i32_e32 vcc, s4, v2
	v_cvt_f32_f16_e32 v2, v33
	v_add_f32_e32 v3, v4, v1
	v_add_f32_e32 v4, v37, v6
	v_cndmask_b32_e32 v1, v1, v3, vcc
	v_or_b32_e32 v3, 10, v25
	v_add_f32_e32 v2, v4, v2
	v_add_f32_e32 v4, v37, v22
	v_max_f32_e32 v2, 0, v2
	v_add_f32_e32 v4, v4, v5
	v_add_u32_e32 v5, s3, v3
	v_add_f32_e32 v2, v1, v2
	v_cmp_gt_i32_e32 vcc, s4, v5
	s_waitcnt lgkmcnt(0)
	v_cvt_f32_f16_e32 v5, v44
	v_max_f32_e32 v4, 0, v4
	v_cndmask_b32_e32 v1, v1, v2, vcc
	v_add_u32_e32 v2, s0, v3
	v_cmp_gt_i32_e32 vcc, s4, v2
	v_cvt_f32_f16_e32 v2, v34
	v_add_f32_e32 v3, v4, v1
	v_add_f32_e32 v4, v37, v7
	v_cndmask_b32_e32 v1, v1, v3, vcc
	v_or_b32_e32 v3, 11, v25
	v_add_f32_e32 v2, v4, v2
	v_add_f32_e32 v4, v37, v23
	v_max_f32_e32 v2, 0, v2
	v_add_f32_e32 v4, v4, v5
	v_add_u32_e32 v5, s3, v3
	v_add_f32_e32 v2, v1, v2
	v_cmp_gt_i32_e32 vcc, s4, v5
	v_max_f32_e32 v4, 0, v4
	s_nop 0
	v_cndmask_b32_e32 v1, v1, v2, vcc
	v_add_u32_e32 v2, s0, v3
	v_add_f32_e32 v3, v4, v1
	v_cmp_gt_i32_e32 vcc, s4, v2
	s_nop 1
	v_cndmask_b32_e32 v1, v1, v3, vcc
	ds_read_u16 v2, v0 offset:30464
	ds_read_u16 v3, v0 offset:21760
	ds_read_u16 v4, v0 offset:22032
	ds_read_u16 v5, v0 offset:22304
	ds_read_u16 v6, v0 offset:22576
	ds_read_u16 v7, v0 offset:23936
	ds_read_u16 v17, v0 offset:24208
	ds_read_u16 v18, v0 offset:24480
	ds_read_u16 v0, v0 offset:24752
	s_waitcnt lgkmcnt(7)
	v_cvt_f32_f16_e32 v3, v3
	v_cvt_f32_f16_e32 v2, v2
	v_add_f32_e32 v3, v8, v3
	v_add_f32_e32 v8, v37, v24
	v_max_f32_e32 v3, 0, v3
	v_add_f32_e32 v2, v8, v2
	v_add_u32_e32 v8, s3, v19
	v_add_f32_e32 v3, v1, v3
	v_cmp_gt_i32_e32 vcc, s4, v8
	v_max_f32_e32 v2, 0, v2
	s_waitcnt lgkmcnt(0)
	v_cvt_f32_f16_e32 v0, v0
	v_cndmask_b32_e32 v1, v1, v3, vcc
	v_add_u32_e32 v3, s0, v19
	v_cmp_gt_i32_e64 s[0:1], s4, v3
	v_cvt_f32_f16_e32 v3, v4
	v_cmp_gt_u32_e32 vcc, 32, v62
	v_add_f32_e32 v2, v2, v1
	s_and_b64 s[0:1], vcc, s[0:1]
	v_cndmask_b32_e64 v1, v1, v2, s[0:1]
	v_add_f32_e32 v2, v37, v9
	v_add_f32_e32 v2, v2, v3
	v_cvt_f32_f16_e32 v4, v5
	v_max_f32_e32 v2, 0, v2
	v_add_u32_e32 v3, 17, v16
	v_add_f32_e32 v2, v1, v2
	v_cmp_gt_i32_e64 s[0:1], s4, v3
	v_add_u32_e32 v3, 18, v16
	s_nop 0
	v_cndmask_b32_e64 v1, v1, v2, s[0:1]
	v_add_f32_e32 v2, v37, v10
	v_add_f32_e32 v2, v2, v4
	v_cvt_f32_f16_e32 v4, v6
	v_max_f32_e32 v2, 0, v2
	v_add_f32_e32 v2, v1, v2
	v_cmp_gt_i32_e64 s[0:1], s4, v3
	v_add_u32_e32 v3, 19, v16
	s_nop 0
	v_cndmask_b32_e64 v1, v1, v2, s[0:1]
	v_add_f32_e32 v2, v37, v11
	v_add_f32_e32 v2, v2, v4
	v_cvt_f32_f16_e32 v4, v7
	v_max_f32_e32 v2, 0, v2
	v_add_f32_e32 v2, v1, v2
	v_cmp_gt_i32_e64 s[0:1], s4, v3
	v_add_u32_e32 v3, 24, v16
	s_nop 0
	v_cndmask_b32_e64 v1, v1, v2, s[0:1]
	v_add_f32_e32 v2, v37, v12
	v_add_f32_e32 v2, v2, v4
	v_cvt_f32_f16_e32 v4, v17
	v_max_f32_e32 v2, 0, v2
	v_add_f32_e32 v2, v1, v2
	v_cmp_gt_i32_e64 s[0:1], s4, v3
	v_add_u32_e32 v3, 25, v16
	s_nop 0
	v_cndmask_b32_e64 v1, v1, v2, s[0:1]
	v_add_f32_e32 v2, v37, v13
	v_add_f32_e32 v2, v2, v4
	v_cvt_f32_f16_e32 v4, v18
	v_max_f32_e32 v2, 0, v2
	v_add_f32_e32 v2, v1, v2
	v_cmp_gt_i32_e64 s[0:1], s4, v3
	v_add_u32_e32 v3, 26, v16
	s_nop 0
	v_cndmask_b32_e64 v1, v1, v2, s[0:1]
	v_add_f32_e32 v2, v37, v14
	v_add_f32_e32 v2, v2, v4
	v_max_f32_e32 v2, 0, v2
	v_add_f32_e32 v2, v1, v2
	v_cmp_gt_i32_e64 s[0:1], s4, v3
	s_nop 1
	v_cndmask_b32_e64 v1, v1, v2, s[0:1]
	v_add_f32_e32 v2, v37, v15
	v_add_f32_e32 v0, v2, v0
	v_max_f32_e32 v0, 0, v0
	v_add_u32_e32 v2, 27, v16
	v_add_f32_e32 v0, v1, v0
	v_cmp_gt_i32_e64 s[0:1], s4, v2
	v_and_b32_e32 v2, 64, v61
	v_add_u32_e32 v2, 64, v2
	v_cndmask_b32_e64 v0, v1, v0, s[0:1]

.Lfast_sum_l2:
	v_mul_u32_u24_e32 v38, 0x440, v63
	v_lshl_add_u32 v38, v36, 1, v38
	ds_read_u16 v39, v38 offset:17408
	ds_read_u16 v40, v38 offset:17680
	ds_read_u16 v41, v38 offset:17952
	ds_read_u16 v42, v38 offset:18224
	ds_read_u16 v43, v38 offset:19584
	ds_read_u16 v44, v38 offset:19856
	ds_read_u16 v45, v38 offset:20128
	ds_read_u16 v46, v38 offset:20400
	ds_read_u16 v47, v38 offset:21760
	ds_read_u16 v48, v38 offset:22032
	ds_read_u16 v49, v38 offset:22304
	ds_read_u16 v50, v38 offset:22576
	ds_read_u16 v51, v38 offset:23936
	v_cmp_gt_u32_e32 vcc, 32, v62
	v_add_f32_e32 v0, v37, v0
	v_add_f32_e32 v1, v37, v1
	v_add_f32_e32 v2, v37, v2
	v_add_f32_e32 v3, v37, v3
	v_add_f32_e32 v4, v37, v4
	v_add_f32_e32 v5, v37, v5
	v_add_f32_e32 v6, v37, v6
	v_add_f32_e32 v7, v37, v7
	v_add_f32_e32 v8, v37, v8
	v_add_f32_e32 v9, v37, v9
	v_add_f32_e32 v10, v37, v10
	v_add_f32_e32 v11, v37, v11
	v_add_f32_e32 v12, v37, v12
	v_add_f32_e32 v13, v37, v13
	v_add_f32_e32 v14, v37, v14
	v_add_f32_e32 v15, v37, v15
	v_add_f32_e32 v16, v37, v16
	v_add_f32_e32 v17, v37, v17
	v_add_f32_e32 v18, v37, v18
	v_add_f32_e32 v19, v37, v19
	v_add_f32_e32 v20, v37, v20
	v_add_f32_e32 v21, v37, v21
	v_add_f32_e32 v22, v37, v22
	v_add_f32_e32 v23, v37, v23
	v_add_f32_e32 v24, v37, v24
	v_mov_b32_e32 v35, 0
	s_waitcnt lgkmcnt(0)
	ds_read_u16 v52, v38 offset:24208
	ds_read_u16 v53, v38 offset:24480
	ds_read_u16 v54, v38 offset:24752
	ds_read_u16 v55, v38 offset:26112
	ds_read_u16 v56, v38 offset:26384
	ds_read_u16 v57, v38 offset:26656
	ds_read_u16 v58, v38 offset:26928
	ds_read_u16 v59, v38 offset:28288
	ds_read_u16 v60, v38 offset:28560
	ds_read_u16 v32, v38 offset:28832
	ds_read_u16 v33, v38 offset:29104
	ds_read_u16 v34, v38 offset:30464
	v_fma_mix_f32 v0, v39, 1.0, v0 op_sel_hi:[1,0,0]
	v_max_f32_e32 v0, 0, v0
	v_add_f32_e32 v35, v35, v0
	v_fma_mix_f32 v1, v40, 1.0, v1 op_sel_hi:[1,0,0]
	v_max_f32_e32 v1, 0, v1
	v_add_f32_e32 v35, v35, v1
	v_fma_mix_f32 v2, v41, 1.0, v2 op_sel_hi:[1,0,0]
	v_max_f32_e32 v2, 0, v2
	v_add_f32_e32 v35, v35, v2
	v_fma_mix_f32 v3, v42, 1.0, v3 op_sel_hi:[1,0,0]
	v_max_f32_e32 v3, 0, v3
	v_add_f32_e32 v35, v35, v3
	v_fma_mix_f32 v4, v43, 1.0, v4 op_sel_hi:[1,0,0]
	v_max_f32_e32 v4, 0, v4
	v_add_f32_e32 v35, v35, v4
	v_fma_mix_f32 v5, v44, 1.0, v5 op_sel_hi:[1,0,0]
	v_max_f32_e32 v5, 0, v5
	v_add_f32_e32 v35, v35, v5
	v_fma_mix_f32 v6, v45, 1.0, v6 op_sel_hi:[1,0,0]
	v_max_f32_e32 v6, 0, v6
	v_add_f32_e32 v35, v35, v6
	v_fma_mix_f32 v7, v46, 1.0, v7 op_sel_hi:[1,0,0]
	v_max_f32_e32 v7, 0, v7
	v_add_f32_e32 v35, v35, v7
	v_fma_mix_f32 v8, v47, 1.0, v8 op_sel_hi:[1,0,0]
	v_max_f32_e32 v8, 0, v8
	v_add_f32_e32 v35, v35, v8
	v_fma_mix_f32 v9, v48, 1.0, v9 op_sel_hi:[1,0,0]
	v_max_f32_e32 v9, 0, v9
	v_add_f32_e32 v35, v35, v9
	v_fma_mix_f32 v10, v49, 1.0, v10 op_sel_hi:[1,0,0]
	v_max_f32_e32 v10, 0, v10
	v_add_f32_e32 v35, v35, v10
	v_fma_mix_f32 v11, v50, 1.0, v11 op_sel_hi:[1,0,0]
	v_max_f32_e32 v11, 0, v11
	v_add_f32_e32 v35, v35, v11
	v_fma_mix_f32 v12, v51, 1.0, v12 op_sel_hi:[1,0,0]
	v_max_f32_e32 v12, 0, v12
	v_add_f32_e32 v35, v35, v12
	s_waitcnt lgkmcnt(0)
	v_fma_mix_f32 v13, v52, 1.0, v13 op_sel_hi:[1,0,0]
	v_max_f32_e32 v13, 0, v13
	v_add_f32_e32 v35, v35, v13
	v_fma_mix_f32 v14, v53, 1.0, v14 op_sel_hi:[1,0,0]
	v_max_f32_e32 v14, 0, v14
	v_add_f32_e32 v35, v35, v14
	v_fma_mix_f32 v15, v54, 1.0, v15 op_sel_hi:[1,0,0]
	v_max_f32_e32 v15, 0, v15
	v_add_f32_e32 v35, v35, v15
	v_fma_mix_f32 v16, v55, 1.0, v16 op_sel_hi:[1,0,0]
	v_max_f32_e32 v16, 0, v16
	v_add_f32_e32 v35, v35, v16
	v_fma_mix_f32 v17, v56, 1.0, v17 op_sel_hi:[1,0,0]
	v_max_f32_e32 v17, 0, v17
	v_add_f32_e32 v35, v35, v17
	v_fma_mix_f32 v18, v57, 1.0, v18 op_sel_hi:[1,0,0]
	v_max_f32_e32 v18, 0, v18
	v_add_f32_e32 v35, v35, v18
	v_fma_mix_f32 v19, v58, 1.0, v19 op_sel_hi:[1,0,0]
	v_max_f32_e32 v19, 0, v19
	v_add_f32_e32 v35, v35, v19
	v_fma_mix_f32 v20, v59, 1.0, v20 op_sel_hi:[1,0,0]
	v_max_f32_e32 v20, 0, v20
	v_add_f32_e32 v35, v35, v20
	v_fma_mix_f32 v21, v60, 1.0, v21 op_sel_hi:[1,0,0]
	v_max_f32_e32 v21, 0, v21
	v_add_f32_e32 v35, v35, v21
	v_fma_mix_f32 v22, v32, 1.0, v22 op_sel_hi:[1,0,0]
	v_max_f32_e32 v22, 0, v22
	v_add_f32_e32 v35, v35, v22
	v_fma_mix_f32 v23, v33, 1.0, v23 op_sel_hi:[1,0,0]
	v_max_f32_e32 v23, 0, v23
	v_add_f32_e32 v35, v35, v23
	v_fma_mix_f32 v24, v34, 1.0, v24 op_sel_hi:[1,0,0]
	v_max_f32_e32 v24, 0, v24
	v_cndmask_b32_e32 v24, 0, v24, vcc
	v_add_f32_e32 v35, v35, v24
	v_and_b32_e32 v2, 64, v61
	v_add_u32_e32 v2, 64, v2
	v_mov_b32_e32 v0, v35
	s_branch .Ljoin_sum_l2

	.amdhsa_kernel _Z8k_layer2PKhPKfPK15HIP_vector_typeIjLj4EEPKjS2_PKDF16_S2_Pf
		.amdhsa_group_segment_fixed_size 39168
		.amdhsa_private_segment_fixed_size 0
		.amdhsa_kernarg_size 64
		.amdhsa_user_sgpr_count 2
		.amdhsa_user_sgpr_dispatch_ptr 0
		.amdhsa_user_sgpr_queue_ptr 0
		.amdhsa_user_sgpr_kernarg_segment_ptr 1
		.amdhsa_user_sgpr_dispatch_id 0
		.amdhsa_user_sgpr_kernarg_preload_length 0
		.amdhsa_user_sgpr_kernarg_preload_offset 0
		.amdhsa_user_sgpr_private_segment_size 0
		.amdhsa_uses_dynamic_stack 0
		.amdhsa_enable_private_segment 0
		.amdhsa_system_sgpr_workgroup_id_x 1
		.amdhsa_system_sgpr_workgroup_id_y 0
		.amdhsa_system_sgpr_workgroup_id_z 0
		.amdhsa_system_sgpr_workgroup_info 0
		.amdhsa_system_vgpr_workitem_id 0
		.amdhsa_next_free_vgpr 112
		.amdhsa_next_free_sgpr 96
		.amdhsa_accum_offset 112
		.amdhsa_reserve_vcc 1
		.amdhsa_float_round_mode_32 0
		.amdhsa_float_round_mode_16_64 0
		.amdhsa_float_denorm_mode_32 3
		.amdhsa_float_denorm_mode_16_64 3
		.amdhsa_dx10_clamp 1
		.amdhsa_ieee_mode 1
		.amdhsa_fp16_overflow 0
		.amdhsa_tg_split 0
		.amdhsa_exception_fp_ieee_invalid_op 0
		.amdhsa_exception_fp_denorm_src 0
		.amdhsa_exception_fp_ieee_div_zero 0
		.amdhsa_exception_fp_ieee_overflow 0
		.amdhsa_exception_fp_ieee_underflow 0
		.amdhsa_exception_fp_ieee_inexact 0
		.amdhsa_exception_int_div_zero 0
	.end_amdhsa_kernel

amdhsa.kernels:
  - .agpr_count:     0
    .args:
      - .actual_access:  read_only
        .address_space:  global
        .offset:         0
        .size:           8
        .value_kind:     global_buffer
      - .actual_access:  read_only
        .address_space:  global
        .offset:         8
        .size:           8
        .value_kind:     global_buffer
      - .actual_access:  write_only
        .address_space:  global
        .offset:         16
        .size:           8
        .value_kind:     global_buffer
      - .actual_access:  write_only
        .address_space:  global
        .offset:         24
        .size:           8
        .value_kind:     global_buffer
      - .actual_access:  read_only
        .address_space:  global
        .offset:         32
        .size:           8
        .value_kind:     global_buffer
      - .actual_access:  read_only
        .address_space:  global
        .offset:         40
        .size:           8
        .value_kind:     global_buffer
      - .actual_access:  read_only
        .address_space:  global
        .offset:         48
        .size:           8
        .value_kind:     global_buffer
      - .actual_access:  read_only
        .address_space:  global
        .offset:         56
        .size:           8
        .value_kind:     global_buffer
      - .actual_access:  read_only
        .address_space:  global
        .offset:         64
        .size:           8
        .value_kind:     global_buffer
      - .actual_access:  write_only
        .address_space:  global
        .offset:         72
        .size:           8
        .value_kind:     global_buffer
      - .actual_access:  write_only
        .address_space:  global
        .offset:         80
        .size:           8
        .value_kind:     global_buffer
      - .actual_access:  write_only
        .address_space:  global
        .offset:         88
        .size:           8
        .value_kind:     global_buffer
      - .actual_access:  write_only
        .address_space:  global
        .offset:         96
        .size:           8
        .value_kind:     global_buffer
      - .actual_access:  write_only
        .address_space:  global
        .offset:         104
        .size:           8
        .value_kind:     global_buffer
      - .actual_access:  write_only
        .address_space:  global
        .offset:         112
        .size:           8
        .value_kind:     global_buffer
      - .offset:         120
        .size:           4
        .value_kind:     hidden_block_count_x
      - .offset:         124
        .size:           4
        .value_kind:     hidden_block_count_y
      - .offset:         128
        .size:           4
        .value_kind:     hidden_block_count_z
      - .offset:         132
        .size:           2
        .value_kind:     hidden_group_size_x
      - .offset:         134
        .size:           2
        .value_kind:     hidden_group_size_y
      - .offset:         136
        .size:           2
        .value_kind:     hidden_group_size_z
      - .offset:         138
        .size:           2
        .value_kind:     hidden_remainder_x
      - .offset:         140
        .size:           2
        .value_kind:     hidden_remainder_y
      - .offset:         142
        .size:           2
        .value_kind:     hidden_remainder_z
      - .offset:         160
        .size:           8
        .value_kind:     hidden_global_offset_x
      - .offset:         168
        .size:           8
        .value_kind:     hidden_global_offset_y
      - .offset:         176
        .size:           8
        .value_kind:     hidden_global_offset_z
      - .offset:         184
        .size:           2
        .value_kind:     hidden_grid_dims
    .group_segment_fixed_size: 21520
    .kernarg_segment_align: 8
    .kernarg_segment_size: 376
    .language:       OpenCL C
    .language_version:
      - 2
      - 0
    .max_flat_workgroup_size: 1024
    .name:           _Z11k_chunksortPKiS0_PjS1_PKfS3_S3_S3_S3_PDF16_S4_PfS5_S4_Ph
    .private_segment_fixed_size: 0
    .sgpr_count:     32
    .sgpr_spill_count: 0
    .symbol:         _Z11k_chunksortPKiS0_PjS1_PKfS3_S3_S3_S3_PDF16_S4_PfS5_S4_Ph.kd
    .uniform_work_group_size: 1
    .uses_dynamic_stack: false
    .vgpr_count:     38
    .vgpr_spill_count: 0
    .wavefront_size: 64
  - .agpr_count:     0
    .args:
      - .actual_access:  read_only
        .address_space:  global
        .offset:         0
        .size:           8
        .value_kind:     global_buffer
      - .actual_access:  read_only
        .address_space:  global
        .offset:         8
        .size:           8
        .value_kind:     global_buffer
      - .actual_access:  read_only
        .address_space:  global
        .offset:         16
        .size:           8
        .value_kind:     global_buffer
      - .actual_access:  write_only
        .address_space:  global
        .offset:         24
        .size:           8
        .value_kind:     global_buffer
      - .actual_access:  write_only
        .address_space:  global
        .offset:         32
        .size:           8
        .value_kind:     global_buffer
      - .actual_access:  write_only
        .address_space:  global
        .offset:         40
        .size:           8
        .value_kind:     global_buffer
      - .actual_access:  write_only
        .address_space:  global
        .offset:         48
        .size:           8
        .value_kind:     global_buffer
    .group_segment_fixed_size: 22536
    .kernarg_segment_align: 8
    .kernarg_segment_size: 56
    .language:       OpenCL C
    .language_version:
      - 2
      - 0
    .max_flat_workgroup_size: 1024
    .name:           _Z5k_csrPKjS0_PKfPjPfPDF16_P15HIP_vector_typeIjLj4EE
    .private_segment_fixed_size: 0
    .sgpr_count:     44
    .sgpr_spill_count: 0
    .symbol:         _Z5k_csrPKjS0_PKfPjPfPDF16_P15HIP_vector_typeIjLj4EE.kd
    .uniform_work_group_size: 1
    .uses_dynamic_stack: false
    .vgpr_count:     48
    .vgpr_spill_count: 0
    .wavefront_size: 64
  - .agpr_count:     0
    .args:
      - .actual_access:  read_only
        .address_space:  global
        .offset:         0
        .size:           8
        .value_kind:     global_buffer
      - .actual_access:  read_only
        .address_space:  global
        .offset:         8
        .size:           8
        .value_kind:     global_buffer
      - .actual_access:  read_only
        .address_space:  global
        .offset:         16
        .size:           8
        .value_kind:     global_buffer
      - .actual_access:  read_only
        .address_space:  global
        .offset:         24
        .size:           8
        .value_kind:     global_buffer
      - .actual_access:  read_only
        .address_space:  global
        .offset:         32
        .size:           8
        .value_kind:     global_buffer
      - .actual_access:  read_only
        .address_space:  global
        .offset:         40
        .size:           8
        .value_kind:     global_buffer
      - .actual_access:  read_only
        .address_space:  global
        .offset:         48
        .size:           8
        .value_kind:     global_buffer
      - .actual_access:  write_only
        .address_space:  global
        .offset:         56
        .size:           8
        .value_kind:     global_buffer
      - .actual_access:  write_only
        .address_space:  global
        .offset:         64
        .size:           8
        .value_kind:     global_buffer
    .group_segment_fixed_size: 36112
    .kernarg_segment_align: 8
    .kernarg_segment_size: 72
    .language:       OpenCL C
    .language_version:
      - 2
      - 0
    .max_flat_workgroup_size: 256
    .name:           _Z8k_layer1PKfPKDF16_PK15HIP_vector_typeIjLj4EEPKjS0_S2_S0_PhPf
    .private_segment_fixed_size: 0
    .sgpr_count:     30
    .sgpr_spill_count: 0
    .symbol:         _Z8k_layer1PKfPKDF16_PK15HIP_vector_typeIjLj4EEPKjS0_S2_S0_PhPf.kd
    .uniform_work_group_size: 1
    .uses_dynamic_stack: false
    .vgpr_count:     128
    .vgpr_spill_count: 0
    .wavefront_size: 64
  - .agpr_count:     0
    .args:
      - .actual_access:  read_only
        .address_space:  global
        .offset:         0
        .size:           8
        .value_kind:     global_buffer
      - .actual_access:  read_only
        .address_space:  global
        .offset:         8
        .size:           8
        .value_kind:     global_buffer
      - .actual_access:  read_only
        .address_space:  global
        .offset:         16
        .size:           8
        .value_kind:     global_buffer
      - .actual_access:  read_only
        .address_space:  global
        .offset:         24
        .size:           8
        .value_kind:     global_buffer
      - .actual_access:  read_only
        .address_space:  global
        .offset:         32
        .size:           8
        .value_kind:     global_buffer
      - .actual_access:  read_only
        .address_space:  global
        .offset:         40
        .size:           8
        .value_kind:     global_buffer
      - .actual_access:  read_only
        .address_space:  global
        .offset:         48
        .size:           8
        .value_kind:     global_buffer
      - .address_space:  global
        .offset:         56
        .size:           8
        .value_kind:     global_buffer
    .group_segment_fixed_size: 39168
    .kernarg_segment_align: 8
    .kernarg_segment_size: 64
    .language:       OpenCL C
    .language_version:
      - 2
      - 0
    .max_flat_workgroup_size: 256
    .name:           _Z8k_layer2PKhPKfPK15HIP_vector_typeIjLj4EEPKjS2_PKDF16_S2_Pf
    .private_segment_fixed_size: 0
    .sgpr_count:     27
    .sgpr_spill_count: 0
    .symbol:         _Z8k_layer2PKhPKfPK15HIP_vector_typeIjLj4EEPKjS2_PKDF16_S2_Pf.kd
    .uniform_work_group_size: 1
    .uses_dynamic_stack: false
    .vgpr_count:     112
    .vgpr_spill_count: 0
    .wavefront_size: 64
  - .agpr_count:     0
    .args:
      - .actual_access:  read_only
        .address_space:  global
        .offset:         0
        .size:           8
        .value_kind:     global_buffer
      - .actual_access:  read_only
        .address_space:  global
        .offset:         8
        .size:           8
        .value_kind:     global_buffer
      - .actual_access:  read_only
        .address_space:  global
        .offset:         16
        .size:           8
        .value_kind:     global_buffer
      - .actual_access:  read_only
        .address_space:  global
        .offset:         24
        .size:           8
        .value_kind:     global_buffer
      - .actual_access:  read_only
        .address_space:  global
        .offset:         32
        .size:           8
        .value_kind:     global_buffer
      - .actual_access:  write_only
        .address_space:  global
        .offset:         40
        .size:           8
        .value_kind:     global_buffer
    .group_segment_fixed_size: 512
    .kernarg_segment_align: 8
    .kernarg_segment_size: 48
    .language:       OpenCL C
    .language_version:
      - 2
      - 0
    .max_flat_workgroup_size: 320
    .name:           _Z7k_headsPKfS0_S0_S0_S0_Pf
    .private_segment_fixed_size: 0
    .sgpr_count:     18
    .sgpr_spill_count: 0
    .symbol:         _Z7k_headsPKfS0_S0_S0_S0_Pf.kd
    .uniform_work_group_size: 1
    .uses_dynamic_stack: false
    .vgpr_count:     56
    .vgpr_spill_count: 0
    .wavefront_size: 64
